# GEMM K-loop back edge rotated: counter and pointer updates moved above the loop-back barrier (8 loops), on top of permlane shuffles
# baseline (speedup 1.0000x reference)
; #define PG8_STAGE(bufoff, gbase, voff) do { _Pragma("unroll") for (int _i = 0; _i < 2; ++_i) \
;         __builtin_amdgcn_global_load_lds((const unsigned*)((const char*)(gbase) + (voff)[_i]), (PG8_LAS unsigned*)(lds + (bufoff) + ldsw + _i * 8192), 16, 0, 0); } while (0)
; #define PG8_WAIT_V(n) asm volatile("s_waitcnt vmcnt(" #n ")" ::: "memory")
; #define PG8_WAIT_L(n) asm volatile("s_waitcnt lgkmcnt(" #n ")" ::: "memory")
; #define PG8_BAR __builtin_amdgcn_s_barrier()
; #define PG8_SCHED __builtin_amdgcn_sched_barrier(0)
; template <class Epi, class Sched, bool ALIGN_EPI = false, bool SP2 = false, bool FP8 = false, bool PEEL = false>
; __device__ __forceinline__ void gemm_phase(PG8_LAS unsigned char* lds, const Gemm g, const Sched& S, const Epi& E, const int wid) {
;     ...
;             const bool last = (t == nt - 2);
;             const char* a1 = cA + (size_t)(t + 1) * kstep;
;             const char* a2 = last ? nA : cA + (size_t)(t + 2) * kstep; const char* b2 = last ? nB : cB + (size_t)(t + 2) * kstep;
;             const char* a3 = a2 + kstep; const char* b3 = b2 + kstep;
;             if (last && has_next) S.a_ready(nxt);
;             PG8_LDB(B0, 0, 0); PG8_LDB(B1, 0, 1); PG8_SCHED; PG8_LDA(At, 0, 0); PG8_STAGE(PG8_SA(1, 1), a1 + hstep, voffA);
;             PG8_WAIT_V(8); PG8_WAIT_L(0); PG8_BAR; PG8_MMA(0, 0, At, B0); PG8_MMA(0, 1, At, B1); PG8_BAR; PG8_SCHED;
;             PG8_LDA(At, 0, 1); PG8_STAGE(PG8_SB(0, 0), b2, voffB); PG8_STAGE(PG8_SB(0, 1), b2 + hstep, voffB); PG8_STAGE(PG8_SA(0, 0), a2, voffA);
.LBB0_237:
	ds_read_b128 v[146:149], v153
	ds_read_b128 v[158:161], v153 offset:1024
	ds_read_b128 v[162:165], v153 offset:2048
	ds_read_b128 v[166:169], v153 offset:3072
	ds_read_b128 v[170:173], v154
	ds_read_b128 v[174:177], v154 offset:1024
	ds_read_b128 v[178:181], v154 offset:2048
	ds_read_b128 v[182:185], v154 offset:3072
	s_add_u32 s30, s36, 0xfffc0080
	s_addc_u32 s31, s37, -1
	s_cmp_eq_u32 s90, 12
	s_cselect_b32 s41, s13, s31
	s_cselect_b32 s40, s21, s30
	s_cselect_b32 s31, s23, s89
	s_cselect_b32 s30, s60, s88
	s_mov_b32 m0, s61
	v_lshl_add_u64 v[140:141], s[36:37], 0, v[136:137]
	ds_read_b128 v[186:189], v155
	ds_read_b128 v[190:193], v155 offset:1024
	ds_read_b128 v[194:197], v155 offset:2048
	ds_read_b128 v[198:201], v155 offset:3072
	ds_read_b128 v[202:205], v155 offset:4096
	ds_read_b128 v[206:209], v155 offset:5120
	ds_read_b128 v[210:213], v155 offset:6144
	ds_read_b128 v[214:217], v155 offset:7168
	global_load_lds_dwordx4 v[140:141], off
	v_lshl_add_u64 v[140:141], s[36:37], 0, v[138:139]
	s_mov_b32 m0, s62
	s_nop 0
	global_load_lds_dwordx4 v[140:141], off
	s_waitcnt vmcnt(8)
	s_waitcnt lgkmcnt(0)
	s_barrier
	s_setprio 1
	s_waitcnt lgkmcnt(0)
	v_mfma_f32_16x16x32_bf16 v[124:127], v[146:149], v[186:189], v[124:127]
	v_mfma_f32_16x16x32_bf16 v[120:123], v[162:165], v[186:189], v[120:123]
	v_mfma_f32_16x16x32_bf16 v[108:111], v[146:149], v[194:197], v[108:111]
	v_mfma_f32_16x16x32_bf16 v[104:107], v[162:165], v[194:197], v[104:107]
	v_mfma_f32_16x16x32_bf16 v[92:95], v[146:149], v[202:205], v[92:95]
	v_mfma_f32_16x16x32_bf16 v[88:91], v[162:165], v[202:205], v[88:91]
	v_mfma_f32_16x16x32_bf16 v[76:79], v[146:149], v[210:213], v[76:79]
	v_mfma_f32_16x16x32_bf16 v[72:75], v[162:165], v[210:213], v[72:75]
	v_mfma_f32_16x16x32_bf16 v[124:127], v[158:161], v[190:193], v[124:127]
	v_mfma_f32_16x16x32_bf16 v[120:123], v[166:169], v[190:193], v[120:123]
	v_mfma_f32_16x16x32_bf16 v[108:111], v[158:161], v[198:201], v[108:111]
	v_mfma_f32_16x16x32_bf16 v[104:107], v[166:169], v[198:201], v[104:107]
	v_mfma_f32_16x16x32_bf16 v[92:95], v[158:161], v[206:209], v[92:95]
	v_mfma_f32_16x16x32_bf16 v[88:91], v[166:169], v[206:209], v[88:91]
	v_mfma_f32_16x16x32_bf16 v[76:79], v[158:161], v[214:217], v[76:79]
	v_mfma_f32_16x16x32_bf16 v[72:75], v[166:169], v[214:217], v[72:75]
	s_setprio 0
	s_setprio 1
	v_mfma_f32_16x16x32_bf16 v[116:119], v[170:173], v[186:189], v[116:119]
	v_mfma_f32_16x16x32_bf16 v[112:115], v[178:181], v[186:189], v[112:115]
	v_mfma_f32_16x16x32_bf16 v[100:103], v[170:173], v[194:197], v[100:103]
	v_mfma_f32_16x16x32_bf16 v[96:99], v[178:181], v[194:197], v[96:99]
	v_mfma_f32_16x16x32_bf16 v[84:87], v[170:173], v[202:205], v[84:87]
	v_mfma_f32_16x16x32_bf16 v[80:83], v[178:181], v[202:205], v[80:83]
	v_mfma_f32_16x16x32_bf16 v[68:71], v[170:173], v[210:213], v[68:71]
	v_mfma_f32_16x16x32_bf16 v[64:67], v[178:181], v[210:213], v[64:67]
	v_mfma_f32_16x16x32_bf16 v[116:119], v[174:177], v[190:193], v[116:119]
	v_mfma_f32_16x16x32_bf16 v[112:115], v[182:185], v[190:193], v[112:115]
	v_mfma_f32_16x16x32_bf16 v[100:103], v[174:177], v[198:201], v[100:103]
	v_mfma_f32_16x16x32_bf16 v[96:99], v[182:185], v[198:201], v[96:99]
	v_mfma_f32_16x16x32_bf16 v[84:87], v[174:177], v[206:209], v[84:87]
	v_mfma_f32_16x16x32_bf16 v[80:83], v[182:185], v[206:209], v[80:83]
	v_mfma_f32_16x16x32_bf16 v[68:71], v[174:177], v[214:217], v[68:71]
	v_mfma_f32_16x16x32_bf16 v[64:67], v[182:185], v[214:217], v[64:67]
	s_setprio 0
	s_barrier
	s_mov_b32 m0, s63
	v_lshl_add_u64 v[140:141], s[30:31], 0, v[130:131]
	s_add_u32 s92, s30, 0x40000
	ds_read_b128 v[186:189], v155 offset:16384
	ds_read_b128 v[190:193], v155 offset:17408
	ds_read_b128 v[194:197], v155 offset:18432
	ds_read_b128 v[198:201], v155 offset:19456
	ds_read_b128 v[202:205], v155 offset:20480
	ds_read_b128 v[206:209], v155 offset:21504
	ds_read_b128 v[210:213], v155 offset:22528
	ds_read_b128 v[214:217], v155 offset:23552
	global_load_lds_dwordx4 v[140:141], off
	v_lshl_add_u64 v[142:143], s[30:31], 0, v[134:135]
	s_mov_b32 m0, s64
	s_addc_u32 s93, s31, 0
	global_load_lds_dwordx4 v[142:143], off
	v_lshl_add_u64 v[218:219], s[92:93], 0, v[130:131]
	s_mov_b32 m0, s65
	v_lshl_add_u64 v[220:221], s[40:41], 0, v[132:133]
	global_load_lds_dwordx4 v[218:219], off
	v_lshl_add_u64 v[218:219], s[92:93], 0, v[134:135]
	s_mov_b32 m0, s66
	s_nop 0
	global_load_lds_dwordx4 v[218:219], off
	v_lshl_add_u64 v[218:219], s[40:41], 0, v[128:129]
	s_mov_b32 m0, s44
	s_nop 0
	global_load_lds_dwordx4 v[218:219], off
	s_mov_b32 m0, s45
	s_nop 0
	global_load_lds_dwordx4 v[220:221], off
	s_waitcnt vmcnt(8)
	s_waitcnt lgkmcnt(0)
	s_barrier
; #define PG8_STAGE(bufoff, gbase, voff) do { _Pragma("unroll") for (int _i = 0; _i < 2; ++_i) \
;         __builtin_amdgcn_global_load_lds((const unsigned*)((const char*)(gbase) + (voff)[_i]), (PG8_LAS unsigned*)(lds + (bufoff) + ldsw + _i * 8192), 16, 0, 0); } while (0)
; #define PG8_WAIT_V(n) asm volatile("s_waitcnt vmcnt(" #n ")" ::: "memory")
; #define PG8_WAIT_L(n) asm volatile("s_waitcnt lgkmcnt(" #n ")" ::: "memory")
; #define PG8_BAR __builtin_amdgcn_s_barrier()
; #define PG8_SCHED __builtin_amdgcn_sched_barrier(0)
; template <class Epi, class Sched, bool ALIGN_EPI = false, bool SP2 = false, bool FP8 = false, bool PEEL = false>
; __device__ __forceinline__ void gemm_phase(PG8_LAS unsigned char* lds, const Gemm g, const Sched& S, const Epi& E, const int wid) {
;     ...
;             PG8_WAIT_V(8); PG8_WAIT_L(0); PG8_BAR; PG8_MMA(1, 0, At, B0); PG8_MMA(1, 1, At, B1); PG8_BAR; PG8_SCHED;
;             PG8_LDB(B0, 1, 0); PG8_LDB(B1, 1, 1); PG8_SCHED; PG8_LDA(At, 1, 0); PG8_STAGE(PG8_SA(0, 1), a2 + hstep, voffA);
;             PG8_WAIT_V(8); PG8_WAIT_L(0); PG8_BAR; PG8_MMA(0, 0, At, B0); PG8_MMA(0, 1, At, B1); PG8_BAR; PG8_SCHED;
	s_setprio 1
	s_waitcnt lgkmcnt(0)
	v_mfma_f32_16x16x32_bf16 v[60:63], v[146:149], v[186:189], v[60:63]
	v_mfma_f32_16x16x32_bf16 v[56:59], v[162:165], v[186:189], v[56:59]
	v_mfma_f32_16x16x32_bf16 v[44:47], v[146:149], v[194:197], v[44:47]
	v_mfma_f32_16x16x32_bf16 v[40:43], v[162:165], v[194:197], v[40:43]
	v_mfma_f32_16x16x32_bf16 v[28:31], v[146:149], v[202:205], v[28:31]
	v_mfma_f32_16x16x32_bf16 v[24:27], v[162:165], v[202:205], v[24:27]
	v_mfma_f32_16x16x32_bf16 v[12:15], v[146:149], v[210:213], v[12:15]
	v_mfma_f32_16x16x32_bf16 v[8:11], v[162:165], v[210:213], v[8:11]
	v_mfma_f32_16x16x32_bf16 v[60:63], v[158:161], v[190:193], v[60:63]
	v_mfma_f32_16x16x32_bf16 v[56:59], v[166:169], v[190:193], v[56:59]
	v_mfma_f32_16x16x32_bf16 v[44:47], v[158:161], v[198:201], v[44:47]
	v_mfma_f32_16x16x32_bf16 v[40:43], v[166:169], v[198:201], v[40:43]
	v_mfma_f32_16x16x32_bf16 v[28:31], v[158:161], v[206:209], v[28:31]
	v_mfma_f32_16x16x32_bf16 v[24:27], v[166:169], v[206:209], v[24:27]
	v_mfma_f32_16x16x32_bf16 v[12:15], v[158:161], v[214:217], v[12:15]
	v_mfma_f32_16x16x32_bf16 v[8:11], v[166:169], v[214:217], v[8:11]
	s_setprio 0
	s_setprio 1
	v_mfma_f32_16x16x32_bf16 v[52:55], v[170:173], v[186:189], v[52:55]
	v_mfma_f32_16x16x32_bf16 v[48:51], v[178:181], v[186:189], v[48:51]
	v_mfma_f32_16x16x32_bf16 v[36:39], v[170:173], v[194:197], v[36:39]
	v_mfma_f32_16x16x32_bf16 v[32:35], v[178:181], v[194:197], v[32:35]
	v_mfma_f32_16x16x32_bf16 v[20:23], v[170:173], v[202:205], v[20:23]
	v_mfma_f32_16x16x32_bf16 v[16:19], v[178:181], v[202:205], v[16:19]
	v_mfma_f32_16x16x32_bf16 v[4:7], v[170:173], v[210:213], v[4:7]
	v_mfma_f32_16x16x32_bf16 v[0:3], v[178:181], v[210:213], v[0:3]
	v_mfma_f32_16x16x32_bf16 v[52:55], v[174:177], v[190:193], v[52:55]
	v_mfma_f32_16x16x32_bf16 v[48:51], v[182:185], v[190:193], v[48:51]
	v_mfma_f32_16x16x32_bf16 v[36:39], v[174:177], v[198:201], v[36:39]
	v_mfma_f32_16x16x32_bf16 v[32:35], v[182:185], v[198:201], v[32:35]
	v_mfma_f32_16x16x32_bf16 v[20:23], v[174:177], v[206:209], v[20:23]
	v_mfma_f32_16x16x32_bf16 v[16:19], v[182:185], v[206:209], v[16:19]
	v_mfma_f32_16x16x32_bf16 v[4:7], v[174:177], v[214:217], v[4:7]
	v_mfma_f32_16x16x32_bf16 v[0:3], v[182:185], v[214:217], v[0:3]
	s_setprio 0
	s_barrier
	ds_read_b128 v[146:149], v144
	ds_read_b128 v[158:161], v144 offset:1024
	ds_read_b128 v[162:165], v144 offset:2048
	ds_read_b128 v[166:169], v144 offset:3072
	ds_read_b128 v[170:173], v145
	ds_read_b128 v[174:177], v145 offset:1024
	ds_read_b128 v[178:181], v145 offset:2048
	ds_read_b128 v[182:185], v145 offset:3072
	s_add_u32 s40, s40, 0x40000
	s_addc_u32 s41, s41, 0
	s_mov_b32 m0, s46
	v_lshl_add_u64 v[222:223], s[40:41], 0, v[128:129]
	ds_read_b128 v[186:189], v155 offset:32768
	ds_read_b128 v[190:193], v155 offset:33792
	ds_read_b128 v[194:197], v155 offset:34816
	ds_read_b128 v[198:201], v155 offset:35840
	ds_read_b128 v[202:205], v155 offset:36864
	ds_read_b128 v[206:209], v155 offset:37888
	ds_read_b128 v[210:213], v155 offset:38912
	ds_read_b128 v[214:217], v155 offset:39936
	global_load_lds_dwordx4 v[222:223], off
	v_lshl_add_u64 v[222:223], s[40:41], 0, v[132:133]
	s_mov_b32 m0, s47
	s_nop 0
	global_load_lds_dwordx4 v[222:223], off
	s_waitcnt vmcnt(8)
	s_waitcnt lgkmcnt(0)
	s_barrier
	s_setprio 1
	s_waitcnt lgkmcnt(0)
	v_mfma_f32_16x16x32_bf16 v[124:127], v[146:149], v[186:189], v[124:127]
	v_mfma_f32_16x16x32_bf16 v[120:123], v[162:165], v[186:189], v[120:123]
	v_mfma_f32_16x16x32_bf16 v[108:111], v[146:149], v[194:197], v[108:111]
	v_mfma_f32_16x16x32_bf16 v[104:107], v[162:165], v[194:197], v[104:107]
	v_mfma_f32_16x16x32_bf16 v[92:95], v[146:149], v[202:205], v[92:95]
	v_mfma_f32_16x16x32_bf16 v[88:91], v[162:165], v[202:205], v[88:91]
	v_mfma_f32_16x16x32_bf16 v[76:79], v[146:149], v[210:213], v[76:79]
	v_mfma_f32_16x16x32_bf16 v[72:75], v[162:165], v[210:213], v[72:75]
	v_mfma_f32_16x16x32_bf16 v[124:127], v[158:161], v[190:193], v[124:127]
	v_mfma_f32_16x16x32_bf16 v[120:123], v[166:169], v[190:193], v[120:123]
	v_mfma_f32_16x16x32_bf16 v[108:111], v[158:161], v[198:201], v[108:111]
	v_mfma_f32_16x16x32_bf16 v[104:107], v[166:169], v[198:201], v[104:107]
	v_mfma_f32_16x16x32_bf16 v[92:95], v[158:161], v[206:209], v[92:95]
	v_mfma_f32_16x16x32_bf16 v[88:91], v[166:169], v[206:209], v[88:91]
	v_mfma_f32_16x16x32_bf16 v[76:79], v[158:161], v[214:217], v[76:79]
	v_mfma_f32_16x16x32_bf16 v[72:75], v[166:169], v[214:217], v[72:75]
	s_setprio 0
	s_setprio 1
	v_mfma_f32_16x16x32_bf16 v[116:119], v[170:173], v[186:189], v[116:119]
	v_mfma_f32_16x16x32_bf16 v[112:115], v[178:181], v[186:189], v[112:115]
	v_mfma_f32_16x16x32_bf16 v[100:103], v[170:173], v[194:197], v[100:103]
	v_mfma_f32_16x16x32_bf16 v[96:99], v[178:181], v[194:197], v[96:99]
	v_mfma_f32_16x16x32_bf16 v[84:87], v[170:173], v[202:205], v[84:87]
	v_mfma_f32_16x16x32_bf16 v[80:83], v[178:181], v[202:205], v[80:83]
	v_mfma_f32_16x16x32_bf16 v[68:71], v[170:173], v[210:213], v[68:71]
	v_mfma_f32_16x16x32_bf16 v[64:67], v[178:181], v[210:213], v[64:67]
	v_mfma_f32_16x16x32_bf16 v[116:119], v[174:177], v[190:193], v[116:119]
	v_mfma_f32_16x16x32_bf16 v[112:115], v[182:185], v[190:193], v[112:115]
	v_mfma_f32_16x16x32_bf16 v[100:103], v[174:177], v[198:201], v[100:103]
	v_mfma_f32_16x16x32_bf16 v[96:99], v[182:185], v[198:201], v[96:99]
	v_mfma_f32_16x16x32_bf16 v[84:87], v[174:177], v[206:209], v[84:87]
	v_mfma_f32_16x16x32_bf16 v[80:83], v[182:185], v[206:209], v[80:83]
	v_mfma_f32_16x16x32_bf16 v[68:71], v[174:177], v[214:217], v[68:71]
	v_mfma_f32_16x16x32_bf16 v[64:67], v[182:185], v[214:217], v[64:67]
	s_setprio 0
	s_barrier
; #define PG8_STAGE(bufoff, gbase, voff) do { _Pragma("unroll") for (int _i = 0; _i < 2; ++_i) \
;         __builtin_amdgcn_global_load_lds((const unsigned*)((const char*)(gbase) + (voff)[_i]), (PG8_LAS unsigned*)(lds + (bufoff) + ldsw + _i * 8192), 16, 0, 0); } while (0)
; #define PG8_WAIT_V(n) asm volatile("s_waitcnt vmcnt(" #n ")" ::: "memory")
; #define PG8_WAIT_L(n) asm volatile("s_waitcnt lgkmcnt(" #n ")" ::: "memory")
; #define PG8_BAR __builtin_amdgcn_s_barrier()
; #define PG8_SCHED __builtin_amdgcn_sched_barrier(0)
; template <class Epi, class Sched, bool ALIGN_EPI = false, bool SP2 = false, bool FP8 = false, bool PEEL = false>
; __device__ __forceinline__ void gemm_phase(PG8_LAS unsigned char* lds, const Gemm g, const Sched& S, const Epi& E, const int wid) {
;     ...
;         for (int t = 2; t < nt; t += 2) {
;     ...
;             PG8_LDA(At, 1, 1); PG8_STAGE(PG8_SB(1, 0), b3, voffB); PG8_STAGE(PG8_SB(1, 1), b3 + hstep, voffB); PG8_STAGE(PG8_SA(1, 0), a3, voffA);
;             PG8_WAIT_V(8); PG8_WAIT_L(0); PG8_BAR; PG8_MMA(1, 0, At, B0); PG8_MMA(1, 1, At, B1); PG8_BAR; PG8_SCHED;
	s_mov_b32 m0, s67
	v_lshl_add_u64 v[140:141], v[140:141], 0, s[14:15]
	s_add_u32 s30, s30, 0x40080
	ds_read_b128 v[186:189], v155 offset:49152
	ds_read_b128 v[190:193], v155 offset:50176
	ds_read_b128 v[194:197], v155 offset:51200
	ds_read_b128 v[198:201], v155 offset:52224
	ds_read_b128 v[202:205], v155 offset:53248
	ds_read_b128 v[206:209], v155 offset:54272
	ds_read_b128 v[210:213], v155 offset:55296
	ds_read_b128 v[214:217], v155 offset:56320
	global_load_lds_dwordx4 v[140:141], off
	v_lshl_add_u64 v[140:141], v[142:143], 0, s[14:15]
	s_mov_b32 m0, s75
	s_addc_u32 s31, s31, 0
	global_load_lds_dwordx4 v[140:141], off
	v_lshl_add_u64 v[140:141], s[30:31], 0, v[130:131]
	s_mov_b32 m0, s84
	s_nop 0
	global_load_lds_dwordx4 v[140:141], off
	v_lshl_add_u64 v[140:141], s[30:31], 0, v[134:135]
	s_mov_b32 m0, s85
	s_nop 0
	global_load_lds_dwordx4 v[140:141], off
	v_lshl_add_u64 v[140:141], v[218:219], 0, s[14:15]
	s_mov_b32 m0, s54
	s_nop 0
	global_load_lds_dwordx4 v[140:141], off
	v_lshl_add_u64 v[140:141], v[220:221], 0, s[14:15]
	s_mov_b32 m0, s55
	s_nop 0
	global_load_lds_dwordx4 v[140:141], off
	s_waitcnt vmcnt(8)
	s_waitcnt lgkmcnt(0)
	s_barrier
	s_setprio 1
	s_waitcnt lgkmcnt(0)
	v_mfma_f32_16x16x32_bf16 v[60:63], v[146:149], v[186:189], v[60:63]
	v_mfma_f32_16x16x32_bf16 v[56:59], v[162:165], v[186:189], v[56:59]
	v_mfma_f32_16x16x32_bf16 v[44:47], v[146:149], v[194:197], v[44:47]
	v_mfma_f32_16x16x32_bf16 v[40:43], v[162:165], v[194:197], v[40:43]
	v_mfma_f32_16x16x32_bf16 v[28:31], v[146:149], v[202:205], v[28:31]
	v_mfma_f32_16x16x32_bf16 v[24:27], v[162:165], v[202:205], v[24:27]
	v_mfma_f32_16x16x32_bf16 v[12:15], v[146:149], v[210:213], v[12:15]
	v_mfma_f32_16x16x32_bf16 v[8:11], v[162:165], v[210:213], v[8:11]
	v_mfma_f32_16x16x32_bf16 v[60:63], v[158:161], v[190:193], v[60:63]
	v_mfma_f32_16x16x32_bf16 v[56:59], v[166:169], v[190:193], v[56:59]
	v_mfma_f32_16x16x32_bf16 v[44:47], v[158:161], v[198:201], v[44:47]
	v_mfma_f32_16x16x32_bf16 v[40:43], v[166:169], v[198:201], v[40:43]
	v_mfma_f32_16x16x32_bf16 v[28:31], v[158:161], v[206:209], v[28:31]
	v_mfma_f32_16x16x32_bf16 v[24:27], v[166:169], v[206:209], v[24:27]
	v_mfma_f32_16x16x32_bf16 v[12:15], v[158:161], v[214:217], v[12:15]
	v_mfma_f32_16x16x32_bf16 v[8:11], v[166:169], v[214:217], v[8:11]
	s_setprio 0
	s_setprio 1
	v_mfma_f32_16x16x32_bf16 v[52:55], v[170:173], v[186:189], v[52:55]
	v_mfma_f32_16x16x32_bf16 v[48:51], v[178:181], v[186:189], v[48:51]
	v_mfma_f32_16x16x32_bf16 v[36:39], v[170:173], v[194:197], v[36:39]
	v_mfma_f32_16x16x32_bf16 v[32:35], v[178:181], v[194:197], v[32:35]
	v_mfma_f32_16x16x32_bf16 v[20:23], v[170:173], v[202:205], v[20:23]
	v_mfma_f32_16x16x32_bf16 v[16:19], v[178:181], v[202:205], v[16:19]
	v_mfma_f32_16x16x32_bf16 v[4:7], v[170:173], v[210:213], v[4:7]
	v_mfma_f32_16x16x32_bf16 v[0:3], v[178:181], v[210:213], v[0:3]
	v_mfma_f32_16x16x32_bf16 v[52:55], v[174:177], v[190:193], v[52:55]
	v_mfma_f32_16x16x32_bf16 v[48:51], v[182:185], v[190:193], v[48:51]
	v_mfma_f32_16x16x32_bf16 v[36:39], v[174:177], v[198:201], v[36:39]
	v_mfma_f32_16x16x32_bf16 v[32:35], v[182:185], v[198:201], v[32:35]
	v_mfma_f32_16x16x32_bf16 v[20:23], v[174:177], v[206:209], v[20:23]
	v_mfma_f32_16x16x32_bf16 v[16:19], v[182:185], v[206:209], v[16:19]
	v_mfma_f32_16x16x32_bf16 v[4:7], v[174:177], v[214:217], v[4:7]
	v_mfma_f32_16x16x32_bf16 v[0:3], v[182:185], v[214:217], v[0:3]
	s_add_i32 s90, s90, 2
	s_add_u32 s36, s36, 0x100
	s_addc_u32 s37, s37, 0
	s_add_u32 s88, s88, 0x100
	s_addc_u32 s89, s89, 0
	s_cmp_gt_u32 s90, 13
	s_setprio 0
	s_barrier
	s_cbranch_scc0 .LBB0_237
	s_and_b64 vcc, exec, s[6:7]
	s_cbranch_vccz .LBB0_240
	s_barrier

; #define PG8_STAGE(bufoff, gbase, voff) do { _Pragma("unroll") for (int _i = 0; _i < 2; ++_i) \
;         __builtin_amdgcn_global_load_lds((const unsigned*)((const char*)(gbase) + (voff)[_i]), (PG8_LAS unsigned*)(lds + (bufoff) + ldsw + _i * 8192), 16, 0, 0); } while (0)
; #define PG8_WAIT_V(n) asm volatile("s_waitcnt vmcnt(" #n ")" ::: "memory")
; #define PG8_WAIT_L(n) asm volatile("s_waitcnt lgkmcnt(" #n ")" ::: "memory")
; #define PG8_BAR __builtin_amdgcn_s_barrier()
; #define PG8_SCHED __builtin_amdgcn_sched_barrier(0)
; template <class Epi, class Sched, bool ALIGN_EPI = false, bool SP2 = false, bool FP8 = false, bool PEEL = false>
; __device__ __forceinline__ void gemm_phase(PG8_LAS unsigned char* lds, const Gemm g, const Sched& S, const Epi& E, const int wid) {
;     ...
;             const bool last = (t == nt - 2);
;             const char* a1 = cA + (size_t)(t + 1) * kstep;
;             const char* a2 = last ? nA : cA + (size_t)(t + 2) * kstep; const char* b2 = last ? nB : cB + (size_t)(t + 2) * kstep;
;             const char* a3 = a2 + kstep; const char* b3 = b2 + kstep;
;             if (last && has_next) S.a_ready(nxt);
;             PG8_LDB(B0, 0, 0); PG8_LDB(B1, 0, 1); PG8_SCHED; PG8_LDA(At, 0, 0); PG8_STAGE(PG8_SA(1, 1), a1 + hstep, voffA);
;             PG8_WAIT_V(8); PG8_WAIT_L(0); PG8_BAR; PG8_MMA(0, 0, At, B0); PG8_MMA(0, 1, At, B1); PG8_BAR; PG8_SCHED;
.LBB0_659:
	v_add_u32_e32 v162, s50, v148
	v_add_u32_e32 v178, s51, v148
	s_add_u32 s26, s6, s24
	ds_read_b128 v[150:153], v162
	ds_read_b128 v[154:157], v162 offset:1024
	ds_read_b128 v[158:161], v162 offset:2048
	ds_read_b128 v[162:165], v162 offset:3072
	ds_read_b128 v[166:169], v178
	ds_read_b128 v[170:173], v178 offset:1024
	ds_read_b128 v[174:177], v178 offset:2048
	ds_read_b128 v[178:181], v178 offset:3072
	s_addc_u32 s27, s7, s25
	s_add_u32 s26, s26, 0x100
	s_addc_u32 s27, s27, 0
	s_add_u32 s59, s54, s24
	s_addc_u32 s60, s55, s25
	s_cmpk_eq_i32 s24, 0x700
	s_cselect_b32 s31, s17, s27
	s_cselect_b32 s30, s56, s26
	s_cselect_b32 s27, s15, s60
	s_cselect_b32 s26, s57, s59
	v_lshl_add_u64 v[218:219], v[144:145], 0, s[24:25]
	s_add_i32 m0, s43, 0xc000
	ds_read_b128 v[182:185], v149
	ds_read_b128 v[190:193], v149 offset:1024
	ds_read_b128 v[194:197], v149 offset:2048
	ds_read_b128 v[198:201], v149 offset:3072
	ds_read_b128 v[202:205], v149 offset:4096
	ds_read_b128 v[206:209], v149 offset:5120
	ds_read_b128 v[210:213], v149 offset:6144
	ds_read_b128 v[214:217], v149 offset:7168
	global_load_lds_dwordx4 v[218:219], off
	v_lshl_add_u64 v[218:219], v[146:147], 0, s[24:25]
	s_add_i32 m0, s43, 0xe000
	s_nop 0
	global_load_lds_dwordx4 v[218:219], off
	s_waitcnt vmcnt(8)
	s_waitcnt lgkmcnt(0)
	s_barrier
	s_setprio 1
	s_waitcnt lgkmcnt(0)
	v_mfma_f32_16x16x32_bf16 v[124:127], v[150:153], v[182:185], v[124:127]
	v_mfma_f32_16x16x32_bf16 v[120:123], v[158:161], v[182:185], v[120:123]
	v_mfma_f32_16x16x32_bf16 v[112:115], v[150:153], v[194:197], v[112:115]
	v_mfma_f32_16x16x32_bf16 v[108:111], v[158:161], v[194:197], v[108:111]
	v_mfma_f32_16x16x32_bf16 v[100:103], v[150:153], v[202:205], v[100:103]
	v_mfma_f32_16x16x32_bf16 v[92:95], v[158:161], v[202:205], v[92:95]
	v_mfma_f32_16x16x32_bf16 v[84:87], v[150:153], v[210:213], v[84:87]
	v_mfma_f32_16x16x32_bf16 v[76:79], v[158:161], v[210:213], v[76:79]
	v_mfma_f32_16x16x32_bf16 v[124:127], v[154:157], v[190:193], v[124:127]
	v_mfma_f32_16x16x32_bf16 v[120:123], v[162:165], v[190:193], v[120:123]
	v_mfma_f32_16x16x32_bf16 v[112:115], v[154:157], v[198:201], v[112:115]
	v_mfma_f32_16x16x32_bf16 v[108:111], v[162:165], v[198:201], v[108:111]
	v_mfma_f32_16x16x32_bf16 v[100:103], v[154:157], v[206:209], v[100:103]
	v_mfma_f32_16x16x32_bf16 v[92:95], v[162:165], v[206:209], v[92:95]
	v_mfma_f32_16x16x32_bf16 v[84:87], v[154:157], v[214:217], v[84:87]
	v_mfma_f32_16x16x32_bf16 v[76:79], v[162:165], v[214:217], v[76:79]
	s_setprio 0
	s_setprio 1
	v_mfma_f32_16x16x32_bf16 v[116:119], v[166:169], v[182:185], v[116:119]
	v_mfma_f32_16x16x32_bf16 v[104:107], v[174:177], v[182:185], v[104:107]
	v_mfma_f32_16x16x32_bf16 v[96:99], v[166:169], v[194:197], v[96:99]
	v_mfma_f32_16x16x32_bf16 v[88:91], v[174:177], v[194:197], v[88:91]
	v_mfma_f32_16x16x32_bf16 v[80:83], v[166:169], v[202:205], v[80:83]
	v_mfma_f32_16x16x32_bf16 v[72:75], v[174:177], v[202:205], v[72:75]
	v_mfma_f32_16x16x32_bf16 v[68:71], v[166:169], v[210:213], v[68:71]
	v_mfma_f32_16x16x32_bf16 v[64:67], v[174:177], v[210:213], v[64:67]
	v_mfma_f32_16x16x32_bf16 v[116:119], v[170:173], v[190:193], v[116:119]
	v_mfma_f32_16x16x32_bf16 v[104:107], v[178:181], v[190:193], v[104:107]
	v_mfma_f32_16x16x32_bf16 v[96:99], v[170:173], v[198:201], v[96:99]
	v_mfma_f32_16x16x32_bf16 v[88:91], v[178:181], v[198:201], v[88:91]
	v_mfma_f32_16x16x32_bf16 v[80:83], v[170:173], v[206:209], v[80:83]
	v_mfma_f32_16x16x32_bf16 v[72:75], v[178:181], v[206:209], v[72:75]
	v_mfma_f32_16x16x32_bf16 v[68:71], v[170:173], v[214:217], v[68:71]
	v_mfma_f32_16x16x32_bf16 v[64:67], v[178:181], v[214:217], v[64:67]
	s_setprio 0
	s_barrier
	s_add_i32 s59, s50, s41
	v_lshl_add_u64 v[218:219], s[26:27], 0, v[132:133]
	s_mov_b32 m0, s59
	ds_read_b128 v[182:185], v149 offset:16384
	ds_read_b128 v[190:193], v149 offset:17408
	ds_read_b128 v[194:197], v149 offset:18432
	ds_read_b128 v[198:201], v149 offset:19456
	ds_read_b128 v[202:205], v149 offset:20480
	ds_read_b128 v[206:209], v149 offset:21504
	ds_read_b128 v[210:213], v149 offset:22528
	ds_read_b128 v[214:217], v149 offset:23552
	global_load_lds_dwordx4 v[218:219], off
	s_add_i32 m0, s59, 0x2000
	s_add_u32 s60, s26, 0x40000
	v_lshl_add_u64 v[220:221], s[26:27], 0, v[128:129]
	s_addc_u32 s61, s27, 0
	s_add_i32 s59, s51, s41
	global_load_lds_dwordx4 v[220:221], off
	v_lshl_add_u64 v[222:223], s[60:61], 0, v[132:133]
	s_mov_b32 m0, s59
	v_lshl_add_u64 v[224:225], s[30:31], 0, v[130:131]
	global_load_lds_dwordx4 v[222:223], off
	v_lshl_add_u64 v[222:223], s[60:61], 0, v[128:129]
	s_add_i32 m0, s59, 0x2000
	s_nop 0
	global_load_lds_dwordx4 v[222:223], off
	v_lshl_add_u64 v[222:223], s[30:31], 0, v[134:135]
	s_mov_b32 m0, s43
	s_nop 0
	global_load_lds_dwordx4 v[222:223], off
	s_mov_b32 m0, s44
	s_nop 0
	global_load_lds_dwordx4 v[224:225], off
	s_waitcnt vmcnt(8)
	s_waitcnt lgkmcnt(0)
	s_barrier
; #define PG8_STAGE(bufoff, gbase, voff) do { _Pragma("unroll") for (int _i = 0; _i < 2; ++_i) \
;         __builtin_amdgcn_global_load_lds((const unsigned*)((const char*)(gbase) + (voff)[_i]), (PG8_LAS unsigned*)(lds + (bufoff) + ldsw + _i * 8192), 16, 0, 0); } while (0)
; #define PG8_WAIT_V(n) asm volatile("s_waitcnt vmcnt(" #n ")" ::: "memory")
; #define PG8_WAIT_L(n) asm volatile("s_waitcnt lgkmcnt(" #n ")" ::: "memory")
; #define PG8_BAR __builtin_amdgcn_s_barrier()
; #define PG8_SCHED __builtin_amdgcn_sched_barrier(0)
; template <class Epi, class Sched, bool ALIGN_EPI = false, bool SP2 = false, bool FP8 = false, bool PEEL = false>
; __device__ __forceinline__ void gemm_phase(PG8_LAS unsigned char* lds, const Gemm g, const Sched& S, const Epi& E, const int wid) {
;     ...
;             PG8_WAIT_V(8); PG8_WAIT_L(0); PG8_BAR; PG8_MMA(0, 0, At, B0); PG8_MMA(0, 1, At, B1); PG8_BAR; PG8_SCHED;
;             PG8_LDA(At, 0, 1); PG8_STAGE(PG8_SB(0, 0), b2, voffB); PG8_STAGE(PG8_SB(0, 1), b2 + hstep, voffB); PG8_STAGE(PG8_SA(0, 0), a2, voffA);
;             PG8_WAIT_V(8); PG8_WAIT_L(0); PG8_BAR; PG8_MMA(1, 0, At, B0); PG8_MMA(1, 1, At, B1); PG8_BAR; PG8_SCHED;
;             PG8_LDB(B0, 1, 0); PG8_LDB(B1, 1, 1); PG8_SCHED; PG8_LDA(At, 1, 0); PG8_STAGE(PG8_SA(0, 1), a2 + hstep, voffA);
;             PG8_WAIT_V(8); PG8_WAIT_L(0); PG8_BAR; PG8_MMA(0, 0, At, B0); PG8_MMA(0, 1, At, B1); PG8_BAR; PG8_SCHED;
;             PG8_LDA(At, 1, 1); PG8_STAGE(PG8_SB(1, 0), b3, voffB); PG8_STAGE(PG8_SB(1, 1), b3 + hstep, voffB); PG8_STAGE(PG8_SA(1, 0), a3, voffA);
	s_setprio 1
	s_waitcnt lgkmcnt(0)
	v_mfma_f32_16x16x32_bf16 v[60:63], v[150:153], v[182:185], v[60:63]
	v_mfma_f32_16x16x32_bf16 v[56:59], v[158:161], v[182:185], v[56:59]
	v_mfma_f32_16x16x32_bf16 v[52:55], v[150:153], v[194:197], v[52:55]
	v_mfma_f32_16x16x32_bf16 v[44:47], v[158:161], v[194:197], v[44:47]
	v_mfma_f32_16x16x32_bf16 v[36:39], v[150:153], v[202:205], v[36:39]
	v_mfma_f32_16x16x32_bf16 v[28:31], v[158:161], v[202:205], v[28:31]
	v_mfma_f32_16x16x32_bf16 v[20:23], v[150:153], v[210:213], v[20:23]
	v_mfma_f32_16x16x32_bf16 v[12:15], v[158:161], v[210:213], v[12:15]
	v_mfma_f32_16x16x32_bf16 v[60:63], v[154:157], v[190:193], v[60:63]
	v_mfma_f32_16x16x32_bf16 v[56:59], v[162:165], v[190:193], v[56:59]
	v_mfma_f32_16x16x32_bf16 v[52:55], v[154:157], v[198:201], v[52:55]
	v_mfma_f32_16x16x32_bf16 v[44:47], v[162:165], v[198:201], v[44:47]
	v_mfma_f32_16x16x32_bf16 v[36:39], v[154:157], v[206:209], v[36:39]
	v_mfma_f32_16x16x32_bf16 v[28:31], v[162:165], v[206:209], v[28:31]
	v_mfma_f32_16x16x32_bf16 v[20:23], v[154:157], v[214:217], v[20:23]
	v_mfma_f32_16x16x32_bf16 v[12:15], v[162:165], v[214:217], v[12:15]
	s_setprio 0
	s_setprio 1
	v_mfma_f32_16x16x32_bf16 v[48:51], v[166:169], v[182:185], v[48:51]
	v_mfma_f32_16x16x32_bf16 v[40:43], v[174:177], v[182:185], v[40:43]
	v_mfma_f32_16x16x32_bf16 v[32:35], v[166:169], v[194:197], v[32:35]
	v_mfma_f32_16x16x32_bf16 v[24:27], v[174:177], v[194:197], v[24:27]
	v_mfma_f32_16x16x32_bf16 v[16:19], v[166:169], v[202:205], v[16:19]
	v_mfma_f32_16x16x32_bf16 v[8:11], v[174:177], v[202:205], v[8:11]
	v_mfma_f32_16x16x32_bf16 v[4:7], v[166:169], v[210:213], v[4:7]
	v_mfma_f32_16x16x32_bf16 v[0:3], v[174:177], v[210:213], v[0:3]
	v_mfma_f32_16x16x32_bf16 v[48:51], v[170:173], v[190:193], v[48:51]
	v_mfma_f32_16x16x32_bf16 v[40:43], v[178:181], v[190:193], v[40:43]
	v_mfma_f32_16x16x32_bf16 v[32:35], v[170:173], v[198:201], v[32:35]
	v_mfma_f32_16x16x32_bf16 v[24:27], v[178:181], v[198:201], v[24:27]
	v_mfma_f32_16x16x32_bf16 v[16:19], v[170:173], v[206:209], v[16:19]
	v_mfma_f32_16x16x32_bf16 v[8:11], v[178:181], v[206:209], v[8:11]
	v_mfma_f32_16x16x32_bf16 v[4:7], v[170:173], v[214:217], v[4:7]
	v_mfma_f32_16x16x32_bf16 v[0:3], v[178:181], v[214:217], v[0:3]
	s_setprio 0
	s_barrier
	s_add_i32 s59, 0, 0x18000
	s_add_i32 s60, 0, 0x1c000
	v_add_u32_e32 v162, s59, v148
	v_add_u32_e32 v178, s60, v148
	ds_read_b128 v[150:153], v162
	ds_read_b128 v[154:157], v162 offset:1024
	ds_read_b128 v[158:161], v162 offset:2048
	ds_read_b128 v[162:165], v162 offset:3072
	ds_read_b128 v[166:169], v178
	ds_read_b128 v[170:173], v178 offset:1024
	ds_read_b128 v[174:177], v178 offset:2048
	ds_read_b128 v[178:181], v178 offset:3072
	s_add_u32 s30, s30, 0x40000
	s_addc_u32 s31, s31, 0
	s_mov_b32 m0, s45
	v_lshl_add_u64 v[226:227], s[30:31], 0, v[134:135]
	ds_read_b128 v[182:185], v149 offset:32768
	ds_read_b128 v[190:193], v149 offset:33792
	ds_read_b128 v[194:197], v149 offset:34816
	ds_read_b128 v[198:201], v149 offset:35840
	ds_read_b128 v[202:205], v149 offset:36864
	ds_read_b128 v[206:209], v149 offset:37888
	ds_read_b128 v[210:213], v149 offset:38912
	ds_read_b128 v[214:217], v149 offset:39936
	global_load_lds_dwordx4 v[226:227], off
	v_lshl_add_u64 v[226:227], s[30:31], 0, v[130:131]
	s_mov_b32 m0, s46
	s_nop 0
	global_load_lds_dwordx4 v[226:227], off
	s_waitcnt vmcnt(8)
	s_waitcnt lgkmcnt(0)
	s_barrier
	s_setprio 1
	s_waitcnt lgkmcnt(0)
	v_mfma_f32_16x16x32_bf16 v[124:127], v[150:153], v[182:185], v[124:127]
	v_mfma_f32_16x16x32_bf16 v[120:123], v[158:161], v[182:185], v[120:123]
	v_mfma_f32_16x16x32_bf16 v[112:115], v[150:153], v[194:197], v[112:115]
	v_mfma_f32_16x16x32_bf16 v[108:111], v[158:161], v[194:197], v[108:111]
	v_mfma_f32_16x16x32_bf16 v[100:103], v[150:153], v[202:205], v[100:103]
	v_mfma_f32_16x16x32_bf16 v[92:95], v[158:161], v[202:205], v[92:95]
	v_mfma_f32_16x16x32_bf16 v[84:87], v[150:153], v[210:213], v[84:87]
	v_mfma_f32_16x16x32_bf16 v[76:79], v[158:161], v[210:213], v[76:79]
	v_mfma_f32_16x16x32_bf16 v[124:127], v[154:157], v[190:193], v[124:127]
	v_mfma_f32_16x16x32_bf16 v[120:123], v[162:165], v[190:193], v[120:123]
	v_mfma_f32_16x16x32_bf16 v[112:115], v[154:157], v[198:201], v[112:115]
	v_mfma_f32_16x16x32_bf16 v[108:111], v[162:165], v[198:201], v[108:111]
	v_mfma_f32_16x16x32_bf16 v[100:103], v[154:157], v[206:209], v[100:103]
	v_mfma_f32_16x16x32_bf16 v[92:95], v[162:165], v[206:209], v[92:95]
	v_mfma_f32_16x16x32_bf16 v[84:87], v[154:157], v[214:217], v[84:87]
	v_mfma_f32_16x16x32_bf16 v[76:79], v[162:165], v[214:217], v[76:79]
	s_setprio 0
	s_setprio 1
	v_mfma_f32_16x16x32_bf16 v[116:119], v[166:169], v[182:185], v[116:119]
	v_mfma_f32_16x16x32_bf16 v[104:107], v[174:177], v[182:185], v[104:107]
	v_mfma_f32_16x16x32_bf16 v[96:99], v[166:169], v[194:197], v[96:99]
	v_mfma_f32_16x16x32_bf16 v[88:91], v[174:177], v[194:197], v[88:91]
	v_mfma_f32_16x16x32_bf16 v[80:83], v[166:169], v[202:205], v[80:83]
	v_mfma_f32_16x16x32_bf16 v[72:75], v[174:177], v[202:205], v[72:75]
	v_mfma_f32_16x16x32_bf16 v[68:71], v[166:169], v[210:213], v[68:71]
	v_mfma_f32_16x16x32_bf16 v[64:67], v[174:177], v[210:213], v[64:67]
	v_mfma_f32_16x16x32_bf16 v[116:119], v[170:173], v[190:193], v[116:119]
	v_mfma_f32_16x16x32_bf16 v[104:107], v[178:181], v[190:193], v[104:107]
	v_mfma_f32_16x16x32_bf16 v[96:99], v[170:173], v[198:201], v[96:99]
	v_mfma_f32_16x16x32_bf16 v[88:91], v[178:181], v[198:201], v[88:91]
	v_mfma_f32_16x16x32_bf16 v[80:83], v[170:173], v[206:209], v[80:83]
	v_mfma_f32_16x16x32_bf16 v[72:75], v[178:181], v[206:209], v[72:75]
	v_mfma_f32_16x16x32_bf16 v[68:71], v[170:173], v[214:217], v[68:71]
	v_mfma_f32_16x16x32_bf16 v[64:67], v[178:181], v[214:217], v[64:67]
	s_setprio 0
	s_barrier
; #define PG8_STAGE(bufoff, gbase, voff) do { _Pragma("unroll") for (int _i = 0; _i < 2; ++_i) \
;         __builtin_amdgcn_global_load_lds((const unsigned*)((const char*)(gbase) + (voff)[_i]), (PG8_LAS unsigned*)(lds + (bufoff) + ldsw + _i * 8192), 16, 0, 0); } while (0)
; #define PG8_WAIT_V(n) asm volatile("s_waitcnt vmcnt(" #n ")" ::: "memory")
; #define PG8_WAIT_L(n) asm volatile("s_waitcnt lgkmcnt(" #n ")" ::: "memory")
; #define PG8_BAR __builtin_amdgcn_s_barrier()
; #define PG8_SCHED __builtin_amdgcn_sched_barrier(0)
; template <class Epi, class Sched, bool ALIGN_EPI = false, bool SP2 = false, bool FP8 = false, bool PEEL = false>
; __device__ __forceinline__ void gemm_phase(PG8_LAS unsigned char* lds, const Gemm g, const Sched& S, const Epi& E, const int wid) {
;     ...
;             PG8_LDA(At, 1, 1); PG8_STAGE(PG8_SB(1, 0), b3, voffB); PG8_STAGE(PG8_SB(1, 1), b3 + hstep, voffB); PG8_STAGE(PG8_SA(1, 0), a3, voffA);
;             PG8_WAIT_V(8); PG8_WAIT_L(0); PG8_BAR; PG8_MMA(1, 0, At, B0); PG8_MMA(1, 1, At, B1); PG8_BAR; PG8_SCHED;
;         }
;     ...
;         if (!has_next) break;
;         if constexpr (!PEEL) {
; #pragma unroll
;         for (int a = 0; a < 2; ++a)
; #pragma unroll
;             for (int b = 0; b < 2; ++b)
; #pragma unroll
;                 for (int m = 0; m < 4; ++m)
; #pragma unroll
;                     for (int n = 0; n < 2; ++n) acc[a][b][m][n] = (f32x4){0.f, 0.f, 0.f, 0.f};
	s_add_i32 s30, s59, s41
	v_lshl_add_u64 v[218:219], v[218:219], 0, s[12:13]
	s_mov_b32 m0, s30
	ds_read_b128 v[182:185], v149 offset:49152
	ds_read_b128 v[190:193], v149 offset:50176
	ds_read_b128 v[194:197], v149 offset:51200
	ds_read_b128 v[198:201], v149 offset:52224
	ds_read_b128 v[202:205], v149 offset:53248
	ds_read_b128 v[206:209], v149 offset:54272
	ds_read_b128 v[210:213], v149 offset:55296
	ds_read_b128 v[214:217], v149 offset:56320
	global_load_lds_dwordx4 v[218:219], off
	s_add_i32 m0, s30, 0x2000
	s_add_u32 s26, s26, 0x40080
	v_lshl_add_u64 v[218:219], v[220:221], 0, s[12:13]
	s_addc_u32 s27, s27, 0
	s_add_i32 s30, s60, s41
	global_load_lds_dwordx4 v[218:219], off
	v_lshl_add_u64 v[218:219], s[26:27], 0, v[132:133]
	s_mov_b32 m0, s30
	s_nop 0
	global_load_lds_dwordx4 v[218:219], off
	v_lshl_add_u64 v[218:219], s[26:27], 0, v[128:129]
	s_add_i32 m0, s30, 0x2000
	s_nop 0
	global_load_lds_dwordx4 v[218:219], off
	v_lshl_add_u64 v[218:219], v[222:223], 0, s[12:13]
	s_mov_b32 m0, s47
	s_nop 0
	global_load_lds_dwordx4 v[218:219], off
	v_lshl_add_u64 v[218:219], v[224:225], 0, s[12:13]
	s_mov_b32 m0, s48
	s_nop 0
	global_load_lds_dwordx4 v[218:219], off
	s_waitcnt vmcnt(8)
	s_waitcnt lgkmcnt(0)
	s_barrier
	s_setprio 1
	s_waitcnt lgkmcnt(0)
	v_mfma_f32_16x16x32_bf16 v[60:63], v[150:153], v[182:185], v[60:63]
	v_mfma_f32_16x16x32_bf16 v[56:59], v[158:161], v[182:185], v[56:59]
	v_mfma_f32_16x16x32_bf16 v[52:55], v[150:153], v[194:197], v[52:55]
	v_mfma_f32_16x16x32_bf16 v[44:47], v[158:161], v[194:197], v[44:47]
	v_mfma_f32_16x16x32_bf16 v[36:39], v[150:153], v[202:205], v[36:39]
	v_mfma_f32_16x16x32_bf16 v[28:31], v[158:161], v[202:205], v[28:31]
	v_mfma_f32_16x16x32_bf16 v[20:23], v[150:153], v[210:213], v[20:23]
	v_mfma_f32_16x16x32_bf16 v[12:15], v[158:161], v[210:213], v[12:15]
	v_mfma_f32_16x16x32_bf16 v[60:63], v[154:157], v[190:193], v[60:63]
	v_mfma_f32_16x16x32_bf16 v[56:59], v[162:165], v[190:193], v[56:59]
	v_mfma_f32_16x16x32_bf16 v[52:55], v[154:157], v[198:201], v[52:55]
	v_mfma_f32_16x16x32_bf16 v[44:47], v[162:165], v[198:201], v[44:47]
	v_mfma_f32_16x16x32_bf16 v[36:39], v[154:157], v[206:209], v[36:39]
	v_mfma_f32_16x16x32_bf16 v[28:31], v[162:165], v[206:209], v[28:31]
	v_mfma_f32_16x16x32_bf16 v[20:23], v[154:157], v[214:217], v[20:23]
	v_mfma_f32_16x16x32_bf16 v[12:15], v[162:165], v[214:217], v[12:15]
	s_setprio 0
	s_setprio 1
	v_mfma_f32_16x16x32_bf16 v[48:51], v[166:169], v[182:185], v[48:51]
	v_mfma_f32_16x16x32_bf16 v[40:43], v[174:177], v[182:185], v[40:43]
	v_mfma_f32_16x16x32_bf16 v[32:35], v[166:169], v[194:197], v[32:35]
	v_mfma_f32_16x16x32_bf16 v[24:27], v[174:177], v[194:197], v[24:27]
	v_mfma_f32_16x16x32_bf16 v[16:19], v[166:169], v[202:205], v[16:19]
	v_mfma_f32_16x16x32_bf16 v[8:11], v[174:177], v[202:205], v[8:11]
	v_mfma_f32_16x16x32_bf16 v[4:7], v[166:169], v[210:213], v[4:7]
	v_mfma_f32_16x16x32_bf16 v[0:3], v[174:177], v[210:213], v[0:3]
	v_mfma_f32_16x16x32_bf16 v[48:51], v[170:173], v[190:193], v[48:51]
	v_mfma_f32_16x16x32_bf16 v[40:43], v[178:181], v[190:193], v[40:43]
	v_mfma_f32_16x16x32_bf16 v[32:35], v[170:173], v[198:201], v[32:35]
	v_mfma_f32_16x16x32_bf16 v[24:27], v[178:181], v[198:201], v[24:27]
	v_mfma_f32_16x16x32_bf16 v[16:19], v[170:173], v[206:209], v[16:19]
	v_mfma_f32_16x16x32_bf16 v[8:11], v[178:181], v[206:209], v[8:11]
	v_mfma_f32_16x16x32_bf16 v[4:7], v[170:173], v[214:217], v[4:7]
	v_mfma_f32_16x16x32_bf16 v[0:3], v[178:181], v[214:217], v[0:3]
	s_add_i32 s58, s58, 2
	s_add_u32 s24, s24, 0x100
	s_addc_u32 s25, s25, 0
	s_cmp_gt_u32 s58, 13
	s_setprio 0
	s_barrier
	s_cbranch_scc0 .LBB0_659
	s_add_u32 s24, s54, 0xffffff00
	s_addc_u32 s25, s55, -1
	s_andn2_b64 vcc, exec, s[10:11]
	s_cbranch_vccnz .LBB0_662
	v_mov_b32_e32 v0, 0
	s_mov_b32 s4, s14
	s_mov_b32 s3, s52
	s_mov_b64 s[6:7], s[22:23]
	s_mov_b32 s49, s53
	v_mov_b32_e32 v1, v0
	v_mov_b32_e32 v2, v0
	v_mov_b32_e32 v3, v0
	v_mov_b32_e32 v4, v0
	v_mov_b32_e32 v5, v0
	v_mov_b32_e32 v6, v0
	v_mov_b32_e32 v7, v0
	v_mov_b32_e32 v8, v0
	v_mov_b32_e32 v9, v0
	v_mov_b32_e32 v10, v0
	v_mov_b32_e32 v11, v0
	v_mov_b32_e32 v16, v0
	v_mov_b32_e32 v17, v0
	v_mov_b32_e32 v18, v0
	v_mov_b32_e32 v19, v0
	v_mov_b32_e32 v24, v0
	v_mov_b32_e32 v25, v0
	v_mov_b32_e32 v26, v0
	v_mov_b32_e32 v27, v0
	v_mov_b32_e32 v32, v0
	v_mov_b32_e32 v33, v0
	v_mov_b32_e32 v34, v0
	v_mov_b32_e32 v35, v0
	v_mov_b32_e32 v40, v0
	v_mov_b32_e32 v41, v0
	v_mov_b32_e32 v42, v0
	v_mov_b32_e32 v43, v0
	v_mov_b32_e32 v48, v0
	v_mov_b32_e32 v49, v0
	v_mov_b32_e32 v50, v0
	v_mov_b32_e32 v51, v0
	v_mov_b32_e32 v12, v0
	v_mov_b32_e32 v13, v0
	v_mov_b32_e32 v14, v0
	v_mov_b32_e32 v15, v0
	v_mov_b32_e32 v20, v0
	v_mov_b32_e32 v21, v0
	v_mov_b32_e32 v22, v0
	v_mov_b32_e32 v23, v0
	v_mov_b32_e32 v28, v0
	v_mov_b32_e32 v29, v0
	v_mov_b32_e32 v30, v0
	v_mov_b32_e32 v31, v0
	v_mov_b32_e32 v36, v0
	v_mov_b32_e32 v37, v0
	v_mov_b32_e32 v38, v0
	v_mov_b32_e32 v39, v0
	v_mov_b32_e32 v44, v0
	v_mov_b32_e32 v45, v0
	v_mov_b32_e32 v46, v0
	v_mov_b32_e32 v47, v0
	v_mov_b32_e32 v52, v0
	v_mov_b32_e32 v53, v0
	v_mov_b32_e32 v54, v0
	v_mov_b32_e32 v55, v0
	v_mov_b32_e32 v56, v0
	v_mov_b32_e32 v57, v0
	v_mov_b32_e32 v58, v0
	v_mov_b32_e32 v59, v0
	v_mov_b32_e32 v60, v0
	v_mov_b32_e32 v61, v0
	v_mov_b32_e32 v62, v0
	v_mov_b32_e32 v63, v0
	v_mov_b32_e32 v64, v0
	v_mov_b32_e32 v65, v0
	v_mov_b32_e32 v66, v0
	v_mov_b32_e32 v67, v0
	v_mov_b32_e32 v68, v0
	v_mov_b32_e32 v69, v0
	v_mov_b32_e32 v70, v0
	v_mov_b32_e32 v71, v0
	v_mov_b32_e32 v72, v0
	v_mov_b32_e32 v73, v0
	v_mov_b32_e32 v74, v0
	v_mov_b32_e32 v75, v0
	v_mov_b32_e32 v80, v0
	v_mov_b32_e32 v81, v0
	v_mov_b32_e32 v82, v0
	v_mov_b32_e32 v83, v0
	v_mov_b32_e32 v88, v0
	v_mov_b32_e32 v89, v0
	v_mov_b32_e32 v90, v0
	v_mov_b32_e32 v91, v0
	v_mov_b32_e32 v96, v0
	v_mov_b32_e32 v97, v0
	v_mov_b32_e32 v98, v0
	v_mov_b32_e32 v99, v0
	v_mov_b32_e32 v104, v0
	v_mov_b32_e32 v105, v0
	v_mov_b32_e32 v106, v0
	v_mov_b32_e32 v107, v0
	v_mov_b32_e32 v116, v0
	v_mov_b32_e32 v117, v0
	v_mov_b32_e32 v118, v0
	v_mov_b32_e32 v119, v0
	v_mov_b32_e32 v76, v0
	v_mov_b32_e32 v77, v0
	v_mov_b32_e32 v78, v0
	v_mov_b32_e32 v79, v0
	v_mov_b32_e32 v84, v0
	v_mov_b32_e32 v85, v0
	v_mov_b32_e32 v86, v0
	v_mov_b32_e32 v87, v0
	v_mov_b32_e32 v92, v0
	v_mov_b32_e32 v93, v0
	v_mov_b32_e32 v94, v0
	v_mov_b32_e32 v95, v0
	v_mov_b32_e32 v100, v0
	v_mov_b32_e32 v101, v0
	v_mov_b32_e32 v102, v0
	v_mov_b32_e32 v103, v0
	v_mov_b32_e32 v108, v0
	v_mov_b32_e32 v109, v0
	v_mov_b32_e32 v110, v0
	v_mov_b32_e32 v111, v0
	v_mov_b32_e32 v112, v0
	v_mov_b32_e32 v113, v0
	v_mov_b32_e32 v114, v0
	v_mov_b32_e32 v115, v0
	v_mov_b32_e32 v120, v0
	v_mov_b32_e32 v121, v0
	v_mov_b32_e32 v122, v0
	v_mov_b32_e32 v123, v0
	v_mov_b32_e32 v124, v0
	v_mov_b32_e32 v125, v0
	v_mov_b32_e32 v126, v0
	v_mov_b32_e32 v127, v0
	s_andn2_b64 vcc, exec, s[8:9]
	s_cbranch_vccnz .LBB0_663
	s_branch .LBB0_664

; #define PG8_STAGE(bufoff, gbase, voff) do { _Pragma("unroll") for (int _i = 0; _i < 2; ++_i) \
;         __builtin_amdgcn_global_load_lds((const unsigned*)((const char*)(gbase) + (voff)[_i]), (PG8_LAS unsigned*)(lds + (bufoff) + ldsw + _i * 8192), 16, 0, 0); } while (0)
; #define PG8_WAIT_V(n) asm volatile("s_waitcnt vmcnt(" #n ")" ::: "memory")
; #define PG8_WAIT_L(n) asm volatile("s_waitcnt lgkmcnt(" #n ")" ::: "memory")
; #define PG8_BAR __builtin_amdgcn_s_barrier()
; #define PG8_SCHED __builtin_amdgcn_sched_barrier(0)
; template <class Epi, class Sched, bool ALIGN_EPI = false, bool SP2 = false, bool FP8 = false, bool PEEL = false>
; __device__ __forceinline__ void gemm_phase(PG8_LAS unsigned char* lds, const Gemm g, const Sched& S, const Epi& E, const int wid) {
;     ...
;             const bool last = (t == nt - 2);
;             const char* a1 = cA + (size_t)(t + 1) * kstep;
;             const char* a2 = last ? nA : cA + (size_t)(t + 2) * kstep; const char* b2 = last ? nB : cB + (size_t)(t + 2) * kstep;
;             const char* a3 = a2 + kstep; const char* b3 = b2 + kstep;
;             if (last && has_next) S.a_ready(nxt);
;             PG8_LDB(B0, 0, 0); PG8_LDB(B1, 0, 1); PG8_SCHED; PG8_LDA(At, 0, 0); PG8_STAGE(PG8_SA(1, 1), a1 + hstep, voffA);
;             PG8_WAIT_V(8); PG8_WAIT_L(0); PG8_BAR; PG8_MMA(0, 0, At, B0); PG8_MMA(0, 1, At, B1); PG8_BAR; PG8_SCHED;
;             PG8_LDA(At, 0, 1); PG8_STAGE(PG8_SB(0, 0), b2, voffB); PG8_STAGE(PG8_SB(0, 1), b2 + hstep, voffB); PG8_STAGE(PG8_SA(0, 0), a2, voffA);
;             PG8_WAIT_V(8); PG8_WAIT_L(0); PG8_BAR; PG8_MMA(1, 0, At, B0); PG8_MMA(1, 1, At, B1); PG8_BAR; PG8_SCHED;
;             PG8_LDB(B0, 1, 0); PG8_LDB(B1, 1, 1); PG8_SCHED; PG8_LDA(At, 1, 0); PG8_STAGE(PG8_SA(0, 1), a2 + hstep, voffA);
;             PG8_WAIT_V(8); PG8_WAIT_L(0); PG8_BAR; PG8_MMA(0, 0, At, B0); PG8_MMA(0, 1, At, B1); PG8_BAR; PG8_SCHED;
.LBB0_867:
	ds_read_b128 v[0:3], v188
	ds_read_b128 v[4:7], v188 offset:1024
	ds_read_b128 v[16:19], v188 offset:2048
	ds_read_b128 v[20:23], v188 offset:3072
	ds_read_b128 v[24:27], v189
	ds_read_b128 v[28:31], v189 offset:1024
	ds_read_b128 v[176:179], v189 offset:2048
	ds_read_b128 v[180:183], v189 offset:3072
	s_add_u32 s44, s46, 0xfffe0080
	s_addc_u32 s45, s47, -1
	s_cmp_eq_u32 s91, 4
	s_cselect_b32 s49, s25, s45
	s_cselect_b32 s48, s27, s44
	s_cselect_b32 s45, s63, s90
	s_cselect_b32 s44, s64, s89
	s_mov_b32 m0, s59
	v_lshl_add_u64 v[216:217], s[46:47], 0, v[168:169]
	ds_read_b128 v[8:11], v187
	ds_read_b128 v[12:15], v187 offset:1024
	ds_read_b128 v[192:195], v187 offset:2048
	ds_read_b128 v[196:199], v187 offset:3072
	ds_read_b128 v[200:203], v187 offset:4096
	ds_read_b128 v[204:207], v187 offset:5120
	ds_read_b128 v[208:211], v187 offset:6144
	ds_read_b128 v[212:215], v187 offset:7168
	global_load_lds_dwordx4 v[216:217], off
	v_lshl_add_u64 v[216:217], s[46:47], 0, v[170:171]
	s_mov_b32 m0, s65
	s_nop 0
	global_load_lds_dwordx4 v[216:217], off
	s_waitcnt vmcnt(8)
	s_waitcnt lgkmcnt(0)
	s_barrier
	s_setprio 1
	s_waitcnt lgkmcnt(0)
	v_mfma_f32_16x16x128_f8f6f4 v[156:159], v[0:7], v[8:15], v[156:159]
	v_mfma_f32_16x16x128_f8f6f4 v[152:155], v[16:23], v[8:15], v[152:155]
	v_mfma_f32_16x16x128_f8f6f4 v[148:151], v[0:7], v[192:199], v[148:151]
	v_mfma_f32_16x16x128_f8f6f4 v[144:147], v[16:23], v[192:199], v[144:147]
	v_mfma_f32_16x16x128_f8f6f4 v[140:143], v[0:7], v[200:207], v[140:143]
	v_mfma_f32_16x16x128_f8f6f4 v[136:139], v[16:23], v[200:207], v[136:139]
	v_mfma_f32_16x16x128_f8f6f4 v[132:135], v[0:7], v[208:215], v[132:135]
	v_mfma_f32_16x16x128_f8f6f4 v[128:131], v[16:23], v[208:215], v[128:131]
	s_setprio 0
	s_setprio 1
	v_mfma_f32_16x16x128_f8f6f4 v[124:127], v[24:31], v[8:15], v[124:127]
	v_mfma_f32_16x16x128_f8f6f4 v[120:123], v[176:183], v[8:15], v[120:123]
	v_mfma_f32_16x16x128_f8f6f4 v[116:119], v[24:31], v[192:199], v[116:119]
	v_mfma_f32_16x16x128_f8f6f4 v[112:115], v[176:183], v[192:199], v[112:115]
	v_mfma_f32_16x16x128_f8f6f4 v[108:111], v[24:31], v[200:207], v[108:111]
	v_mfma_f32_16x16x128_f8f6f4 v[104:107], v[176:183], v[200:207], v[104:107]
	v_mfma_f32_16x16x128_f8f6f4 v[100:103], v[24:31], v[208:215], v[100:103]
	v_mfma_f32_16x16x128_f8f6f4 v[96:99], v[176:183], v[208:215], v[96:99]
	s_setprio 0
	s_barrier
	s_mov_b32 m0, s66
	v_lshl_add_u64 v[8:9], s[44:45], 0, v[164:165]
	s_add_u32 s92, s44, 0x20000
	ds_read_b128 v[192:195], v187 offset:16384
	ds_read_b128 v[196:199], v187 offset:17408
	ds_read_b128 v[200:203], v187 offset:18432
	ds_read_b128 v[204:207], v187 offset:19456
	ds_read_b128 v[208:211], v187 offset:20480
	ds_read_b128 v[212:215], v187 offset:21504
	ds_read_b128 v[216:219], v187 offset:22528
	ds_read_b128 v[220:223], v187 offset:23552
	global_load_lds_dwordx4 v[8:9], off
	v_lshl_add_u64 v[10:11], s[44:45], 0, v[160:161]
	s_mov_b32 m0, s67
	s_addc_u32 s93, s45, 0
	global_load_lds_dwordx4 v[10:11], off
	v_lshl_add_u64 v[12:13], s[92:93], 0, v[164:165]
	s_mov_b32 m0, s75
	v_lshl_add_u64 v[14:15], s[48:49], 0, v[162:163]
	global_load_lds_dwordx4 v[12:13], off
	v_lshl_add_u64 v[12:13], s[92:93], 0, v[160:161]
	s_mov_b32 m0, s84
	s_nop 0
	global_load_lds_dwordx4 v[12:13], off
	v_lshl_add_u64 v[12:13], s[48:49], 0, v[166:167]
	s_mov_b32 m0, s42
	s_nop 0
	global_load_lds_dwordx4 v[12:13], off
	s_mov_b32 m0, s43
	s_nop 0
	global_load_lds_dwordx4 v[14:15], off
	s_waitcnt vmcnt(8)
	s_waitcnt lgkmcnt(0)
	s_barrier
	s_setprio 1
	s_waitcnt lgkmcnt(0)
	v_mfma_f32_16x16x128_f8f6f4 v[92:95], v[0:7], v[192:199], v[92:95]
	v_mfma_f32_16x16x128_f8f6f4 v[88:91], v[16:23], v[192:199], v[88:91]
	v_mfma_f32_16x16x128_f8f6f4 v[84:87], v[0:7], v[200:207], v[84:87]
	v_mfma_f32_16x16x128_f8f6f4 v[80:83], v[16:23], v[200:207], v[80:83]
	v_mfma_f32_16x16x128_f8f6f4 v[76:79], v[0:7], v[208:215], v[76:79]
	v_mfma_f32_16x16x128_f8f6f4 v[72:75], v[16:23], v[208:215], v[72:75]
	v_mfma_f32_16x16x128_f8f6f4 v[68:71], v[0:7], v[216:223], v[68:71]
	v_mfma_f32_16x16x128_f8f6f4 v[64:67], v[16:23], v[216:223], v[64:67]
	s_setprio 0
	s_setprio 1
	v_mfma_f32_16x16x128_f8f6f4 v[60:63], v[24:31], v[192:199], v[60:63]
	v_mfma_f32_16x16x128_f8f6f4 v[56:59], v[176:183], v[192:199], v[56:59]
	v_mfma_f32_16x16x128_f8f6f4 v[52:55], v[24:31], v[200:207], v[52:55]
	v_mfma_f32_16x16x128_f8f6f4 v[48:51], v[176:183], v[200:207], v[48:51]
	v_mfma_f32_16x16x128_f8f6f4 v[44:47], v[24:31], v[208:215], v[44:47]
	v_mfma_f32_16x16x128_f8f6f4 v[40:43], v[176:183], v[208:215], v[40:43]
	v_mfma_f32_16x16x128_f8f6f4 v[36:39], v[24:31], v[216:223], v[36:39]
	v_mfma_f32_16x16x128_f8f6f4 v[32:35], v[176:183], v[216:223], v[32:35]
	s_setprio 0
	s_barrier
; #define PG8_STAGE(bufoff, gbase, voff) do { _Pragma("unroll") for (int _i = 0; _i < 2; ++_i) \
;         __builtin_amdgcn_global_load_lds((const unsigned*)((const char*)(gbase) + (voff)[_i]), (PG8_LAS unsigned*)(lds + (bufoff) + ldsw + _i * 8192), 16, 0, 0); } while (0)
; #define PG8_WAIT_V(n) asm volatile("s_waitcnt vmcnt(" #n ")" ::: "memory")
; #define PG8_WAIT_L(n) asm volatile("s_waitcnt lgkmcnt(" #n ")" ::: "memory")
; #define PG8_BAR __builtin_amdgcn_s_barrier()
; #define PG8_SCHED __builtin_amdgcn_sched_barrier(0)
; template <class Epi, class Sched, bool ALIGN_EPI = false, bool SP2 = false, bool FP8 = false, bool PEEL = false>
; __device__ __forceinline__ void gemm_phase(PG8_LAS unsigned char* lds, const Gemm g, const Sched& S, const Epi& E, const int wid) {
;     ...
;         for (int t = 2; t < nt; t += 2) {
;     ...
;             PG8_LDB(B0, 1, 0); PG8_LDB(B1, 1, 1); PG8_SCHED; PG8_LDA(At, 1, 0); PG8_STAGE(PG8_SA(0, 1), a2 + hstep, voffA);
;             PG8_WAIT_V(8); PG8_WAIT_L(0); PG8_BAR; PG8_MMA(0, 0, At, B0); PG8_MMA(0, 1, At, B1); PG8_BAR; PG8_SCHED;
;             PG8_LDA(At, 1, 1); PG8_STAGE(PG8_SB(1, 0), b3, voffB); PG8_STAGE(PG8_SB(1, 1), b3 + hstep, voffB); PG8_STAGE(PG8_SA(1, 0), a3, voffA);
;             PG8_WAIT_V(8); PG8_WAIT_L(0); PG8_BAR; PG8_MMA(1, 0, At, B0); PG8_MMA(1, 1, At, B1); PG8_BAR; PG8_SCHED;
	ds_read_b128 v[16:19], v190
	ds_read_b128 v[20:23], v190 offset:1024
	ds_read_b128 v[24:27], v190 offset:2048
	ds_read_b128 v[28:31], v190 offset:3072
	ds_read_b128 v[0:3], v191
	ds_read_b128 v[4:7], v191 offset:1024
	ds_read_b128 v[176:179], v191 offset:2048
	ds_read_b128 v[180:183], v191 offset:3072
	s_add_u32 s48, s48, 0x20000
	s_addc_u32 s49, s49, 0
	s_mov_b32 m0, s50
	v_lshl_add_u64 v[224:225], s[48:49], 0, v[166:167]
	ds_read_b128 v[192:195], v187 offset:32768
	ds_read_b128 v[196:199], v187 offset:33792
	ds_read_b128 v[200:203], v187 offset:34816
	ds_read_b128 v[204:207], v187 offset:35840
	ds_read_b128 v[208:211], v187 offset:36864
	ds_read_b128 v[212:215], v187 offset:37888
	ds_read_b128 v[216:219], v187 offset:38912
	ds_read_b128 v[220:223], v187 offset:39936
	global_load_lds_dwordx4 v[224:225], off
	v_lshl_add_u64 v[224:225], s[48:49], 0, v[162:163]
	s_mov_b32 m0, s51
	s_nop 0
	global_load_lds_dwordx4 v[224:225], off
	s_waitcnt vmcnt(8)
	s_waitcnt lgkmcnt(0)
	s_barrier
	s_setprio 1
	s_waitcnt lgkmcnt(0)
	v_mfma_f32_16x16x128_f8f6f4 v[156:159], v[16:23], v[192:199], v[156:159]
	v_mfma_f32_16x16x128_f8f6f4 v[152:155], v[24:31], v[192:199], v[152:155]
	v_mfma_f32_16x16x128_f8f6f4 v[148:151], v[16:23], v[200:207], v[148:151]
	v_mfma_f32_16x16x128_f8f6f4 v[144:147], v[24:31], v[200:207], v[144:147]
	v_mfma_f32_16x16x128_f8f6f4 v[140:143], v[16:23], v[208:215], v[140:143]
	v_mfma_f32_16x16x128_f8f6f4 v[136:139], v[24:31], v[208:215], v[136:139]
	v_mfma_f32_16x16x128_f8f6f4 v[132:135], v[16:23], v[216:223], v[132:135]
	v_mfma_f32_16x16x128_f8f6f4 v[128:131], v[24:31], v[216:223], v[128:131]
	s_setprio 0
	s_setprio 1
	v_mfma_f32_16x16x128_f8f6f4 v[124:127], v[0:7], v[192:199], v[124:127]
	v_mfma_f32_16x16x128_f8f6f4 v[120:123], v[176:183], v[192:199], v[120:123]
	v_mfma_f32_16x16x128_f8f6f4 v[116:119], v[0:7], v[200:207], v[116:119]
	v_mfma_f32_16x16x128_f8f6f4 v[112:115], v[176:183], v[200:207], v[112:115]
	v_mfma_f32_16x16x128_f8f6f4 v[108:111], v[0:7], v[208:215], v[108:111]
	v_mfma_f32_16x16x128_f8f6f4 v[104:107], v[176:183], v[208:215], v[104:107]
	v_mfma_f32_16x16x128_f8f6f4 v[100:103], v[0:7], v[216:223], v[100:103]
	v_mfma_f32_16x16x128_f8f6f4 v[96:99], v[176:183], v[216:223], v[96:99]
	s_setprio 0
	s_barrier
	s_mov_b32 m0, s85
	v_lshl_add_u64 v[8:9], v[8:9], 0, s[10:11]
	s_add_u32 s44, s44, 0x20080
	ds_read_b128 v[192:195], v187 offset:49152
	ds_read_b128 v[196:199], v187 offset:50176
	ds_read_b128 v[200:203], v187 offset:51200
	ds_read_b128 v[204:207], v187 offset:52224
	ds_read_b128 v[208:211], v187 offset:53248
	ds_read_b128 v[212:215], v187 offset:54272
	ds_read_b128 v[216:219], v187 offset:55296
	ds_read_b128 v[220:223], v187 offset:56320
	global_load_lds_dwordx4 v[8:9], off
	v_lshl_add_u64 v[8:9], v[10:11], 0, s[10:11]
	s_mov_b32 m0, s86
	s_addc_u32 s45, s45, 0
	global_load_lds_dwordx4 v[8:9], off
	v_lshl_add_u64 v[8:9], s[44:45], 0, v[164:165]
	s_mov_b32 m0, s87
	s_nop 0
	global_load_lds_dwordx4 v[8:9], off
	v_lshl_add_u64 v[8:9], s[44:45], 0, v[160:161]
	s_mov_b32 m0, s88
	s_nop 0
	global_load_lds_dwordx4 v[8:9], off
	v_lshl_add_u64 v[8:9], v[12:13], 0, s[10:11]
	s_mov_b32 m0, s54
	s_nop 0
	global_load_lds_dwordx4 v[8:9], off
	v_lshl_add_u64 v[8:9], v[14:15], 0, s[10:11]
	s_mov_b32 m0, s55
	s_nop 0
	global_load_lds_dwordx4 v[8:9], off
	s_waitcnt vmcnt(8)
	s_waitcnt lgkmcnt(0)
	s_barrier
	s_setprio 1
	s_waitcnt lgkmcnt(0)
	v_mfma_f32_16x16x128_f8f6f4 v[92:95], v[16:23], v[192:199], v[92:95]
	v_mfma_f32_16x16x128_f8f6f4 v[88:91], v[24:31], v[192:199], v[88:91]
	v_mfma_f32_16x16x128_f8f6f4 v[84:87], v[16:23], v[200:207], v[84:87]
	v_mfma_f32_16x16x128_f8f6f4 v[80:83], v[24:31], v[200:207], v[80:83]
	v_mfma_f32_16x16x128_f8f6f4 v[76:79], v[16:23], v[208:215], v[76:79]
	v_mfma_f32_16x16x128_f8f6f4 v[72:75], v[24:31], v[208:215], v[72:75]
	v_mfma_f32_16x16x128_f8f6f4 v[68:71], v[16:23], v[216:223], v[68:71]
	v_mfma_f32_16x16x128_f8f6f4 v[64:67], v[24:31], v[216:223], v[64:67]
	s_setprio 0
	s_setprio 1
	v_mfma_f32_16x16x128_f8f6f4 v[60:63], v[0:7], v[192:199], v[60:63]
	v_mfma_f32_16x16x128_f8f6f4 v[56:59], v[176:183], v[192:199], v[56:59]
	v_mfma_f32_16x16x128_f8f6f4 v[52:55], v[0:7], v[200:207], v[52:55]
	v_mfma_f32_16x16x128_f8f6f4 v[48:51], v[176:183], v[200:207], v[48:51]
	v_mfma_f32_16x16x128_f8f6f4 v[44:47], v[0:7], v[208:215], v[44:47]
	v_mfma_f32_16x16x128_f8f6f4 v[40:43], v[176:183], v[208:215], v[40:43]
	v_mfma_f32_16x16x128_f8f6f4 v[36:39], v[0:7], v[216:223], v[36:39]
	v_mfma_f32_16x16x128_f8f6f4 v[32:35], v[176:183], v[216:223], v[32:35]
	s_add_i32 s91, s91, 2
	s_add_u32 s46, s46, 0x100
	s_addc_u32 s47, s47, 0
	s_add_u32 s89, s89, 0x100
	s_addc_u32 s90, s90, 0
	s_cmp_gt_u32 s91, 5
	s_setprio 0
	s_barrier
	s_cbranch_scc0 .LBB0_867
	s_and_b64 vcc, exec, s[6:7]
	s_cbranch_vccz .LBB0_870
	s_barrier

; #define PG8_STAGE(bufoff, gbase, voff) do { _Pragma("unroll") for (int _i = 0; _i < 2; ++_i) \
;         __builtin_amdgcn_global_load_lds((const unsigned*)((const char*)(gbase) + (voff)[_i]), (PG8_LAS unsigned*)(lds + (bufoff) + ldsw + _i * 8192), 16, 0, 0); } while (0)
; #define PG8_WAIT_V(n) asm volatile("s_waitcnt vmcnt(" #n ")" ::: "memory")
; #define PG8_WAIT_L(n) asm volatile("s_waitcnt lgkmcnt(" #n ")" ::: "memory")
; #define PG8_BAR __builtin_amdgcn_s_barrier()
; #define PG8_SCHED __builtin_amdgcn_sched_barrier(0)
; template <class Epi, class Sched, bool ALIGN_EPI = false, bool SP2 = false, bool FP8 = false, bool PEEL = false>
; __device__ __forceinline__ void gemm_phase(PG8_LAS unsigned char* lds, const Gemm g, const Sched& S, const Epi& E, const int wid) {
;     ...
;             const bool last = (t == nt - 2);
;             const char* a1 = cA + (size_t)(t + 1) * kstep;
;             const char* a2 = last ? nA : cA + (size_t)(t + 2) * kstep; const char* b2 = last ? nB : cB + (size_t)(t + 2) * kstep;
;             const char* a3 = a2 + kstep; const char* b3 = b2 + kstep;
;             if (last && has_next) S.a_ready(nxt);
;             PG8_LDB(B0, 0, 0); PG8_LDB(B1, 0, 1); PG8_SCHED; PG8_LDA(At, 0, 0); PG8_STAGE(PG8_SA(1, 1), a1 + hstep, voffA);
;             PG8_WAIT_V(8); PG8_WAIT_L(0); PG8_BAR; PG8_MMA(0, 0, At, B0); PG8_MMA(0, 1, At, B1); PG8_BAR; PG8_SCHED;
;             PG8_LDA(At, 0, 1); PG8_STAGE(PG8_SB(0, 0), b2, voffB); PG8_STAGE(PG8_SB(0, 1), b2 + hstep, voffB); PG8_STAGE(PG8_SA(0, 0), a2, voffA);
;             PG8_WAIT_V(8); PG8_WAIT_L(0); PG8_BAR; PG8_MMA(1, 0, At, B0); PG8_MMA(1, 1, At, B1); PG8_BAR; PG8_SCHED;
;             PG8_LDB(B0, 1, 0); PG8_LDB(B1, 1, 1); PG8_SCHED; PG8_LDA(At, 1, 0); PG8_STAGE(PG8_SA(0, 1), a2 + hstep, voffA);
;             PG8_WAIT_V(8); PG8_WAIT_L(0); PG8_BAR; PG8_MMA(0, 0, At, B0); PG8_MMA(0, 1, At, B1); PG8_BAR; PG8_SCHED;
.LBB0_976:
	v_add_u32_e32 v12, s50, v180
	v_add_u32_e32 v172, s51, v180
	s_add_u32 s26, s6, s24
	ds_read_b128 v[0:3], v12
	ds_read_b128 v[4:7], v12 offset:1024
	ds_read_b128 v[8:11], v12 offset:2048
	ds_read_b128 v[12:15], v12 offset:3072
	ds_read_b128 v[16:19], v172
	ds_read_b128 v[20:23], v172 offset:1024
	ds_read_b128 v[182:185], v172 offset:2048
	ds_read_b128 v[186:189], v172 offset:3072
	s_addc_u32 s27, s7, s25
	s_add_u32 s26, s26, 0x100
	s_addc_u32 s27, s27, 0
	s_add_u32 s59, s56, s24
	s_addc_u32 s60, s57, s25
	s_cmpk_eq_i32 s24, 0xd00
	s_cselect_b32 s31, s17, s27
	s_cselect_b32 s30, s16, s26
	s_cselect_b32 s27, s13, s60
	s_cselect_b32 s26, s12, s59
	v_lshl_add_u64 v[198:199], v[168:169], 0, s[24:25]
	s_add_i32 m0, s43, 0xc000
	ds_read_b128 v[172:175], v181
	ds_read_b128 v[176:179], v181 offset:1024
	ds_read_b128 v[190:193], v181 offset:2048
	ds_read_b128 v[194:197], v181 offset:3072
	ds_read_b128 v[206:209], v181 offset:4096
	ds_read_b128 v[210:213], v181 offset:5120
	ds_read_b128 v[214:217], v181 offset:6144
	ds_read_b128 v[218:221], v181 offset:7168
	global_load_lds_dwordx4 v[198:199], off
	v_lshl_add_u64 v[198:199], v[170:171], 0, s[24:25]
	s_add_i32 m0, s43, 0xe000
	s_nop 0
	global_load_lds_dwordx4 v[198:199], off
	s_waitcnt vmcnt(8)
	s_waitcnt lgkmcnt(0)
	s_barrier
	s_setprio 1
	s_waitcnt lgkmcnt(0)
	v_mfma_f32_16x16x128_f8f6f4 v[148:151], v[0:7], v[172:179], v[148:151]
	v_mfma_f32_16x16x128_f8f6f4 v[144:147], v[8:15], v[172:179], v[144:147]
	v_mfma_f32_16x16x128_f8f6f4 v[136:139], v[0:7], v[190:197], v[136:139]
	v_mfma_f32_16x16x128_f8f6f4 v[128:131], v[8:15], v[190:197], v[128:131]
	v_mfma_f32_16x16x128_f8f6f4 v[120:123], v[0:7], v[206:213], v[120:123]
	v_mfma_f32_16x16x128_f8f6f4 v[112:115], v[8:15], v[206:213], v[112:115]
	v_mfma_f32_16x16x128_f8f6f4 v[104:107], v[0:7], v[214:221], v[104:107]
	v_mfma_f32_16x16x128_f8f6f4 v[96:99], v[8:15], v[214:221], v[96:99]
	s_setprio 0
	s_setprio 1
	v_mfma_f32_16x16x128_f8f6f4 v[140:143], v[16:23], v[172:179], v[140:143]
	v_mfma_f32_16x16x128_f8f6f4 v[132:135], v[182:189], v[172:179], v[132:135]
	v_mfma_f32_16x16x128_f8f6f4 v[124:127], v[16:23], v[190:197], v[124:127]
	v_mfma_f32_16x16x128_f8f6f4 v[116:119], v[182:189], v[190:197], v[116:119]
	v_mfma_f32_16x16x128_f8f6f4 v[108:111], v[16:23], v[206:213], v[108:111]
	v_mfma_f32_16x16x128_f8f6f4 v[100:103], v[182:189], v[206:213], v[100:103]
	v_mfma_f32_16x16x128_f8f6f4 v[92:95], v[16:23], v[214:221], v[92:95]
	v_mfma_f32_16x16x128_f8f6f4 v[88:91], v[182:189], v[214:221], v[88:91]
	s_setprio 0
	s_barrier
	s_add_i32 s59, s50, s40
	v_lshl_add_u64 v[172:173], s[26:27], 0, v[156:157]
	s_mov_b32 m0, s59
	ds_read_b128 v[190:193], v181 offset:16384
	ds_read_b128 v[194:197], v181 offset:17408
	ds_read_b128 v[206:209], v181 offset:18432
	ds_read_b128 v[210:213], v181 offset:19456
	ds_read_b128 v[214:217], v181 offset:20480
	ds_read_b128 v[218:221], v181 offset:21504
	ds_read_b128 v[222:225], v181 offset:22528
	ds_read_b128 v[226:229], v181 offset:23552
	global_load_lds_dwordx4 v[172:173], off
	s_add_i32 m0, s59, 0x2000
	s_add_u32 s60, s26, 0x70000
	v_lshl_add_u64 v[174:175], s[26:27], 0, v[152:153]
	s_addc_u32 s61, s27, 0
	s_add_i32 s59, s51, s40
	global_load_lds_dwordx4 v[174:175], off
	v_lshl_add_u64 v[176:177], s[60:61], 0, v[156:157]
	s_mov_b32 m0, s59
	v_lshl_add_u64 v[178:179], s[30:31], 0, v[154:155]
	global_load_lds_dwordx4 v[176:177], off
	v_lshl_add_u64 v[176:177], s[60:61], 0, v[152:153]
	s_add_i32 m0, s59, 0x2000
	s_nop 0
	global_load_lds_dwordx4 v[176:177], off
	v_lshl_add_u64 v[176:177], s[30:31], 0, v[158:159]
	s_mov_b32 m0, s43
	s_nop 0
	global_load_lds_dwordx4 v[176:177], off
	s_mov_b32 m0, s44
	s_nop 0
	global_load_lds_dwordx4 v[178:179], off
	s_waitcnt vmcnt(8)
	s_waitcnt lgkmcnt(0)
	s_barrier
	s_setprio 1
	s_waitcnt lgkmcnt(0)
	v_mfma_f32_16x16x128_f8f6f4 v[84:87], v[0:7], v[190:197], v[84:87]
	v_mfma_f32_16x16x128_f8f6f4 v[80:83], v[8:15], v[190:197], v[80:83]
	v_mfma_f32_16x16x128_f8f6f4 v[72:75], v[0:7], v[206:213], v[72:75]
	v_mfma_f32_16x16x128_f8f6f4 v[64:67], v[8:15], v[206:213], v[64:67]
	v_mfma_f32_16x16x128_f8f6f4 v[56:59], v[0:7], v[214:221], v[56:59]
	v_mfma_f32_16x16x128_f8f6f4 v[48:51], v[8:15], v[214:221], v[48:51]
	v_mfma_f32_16x16x128_f8f6f4 v[40:43], v[0:7], v[222:229], v[40:43]
	v_mfma_f32_16x16x128_f8f6f4 v[32:35], v[8:15], v[222:229], v[32:35]
	s_setprio 0
	s_setprio 1
	v_mfma_f32_16x16x128_f8f6f4 v[76:79], v[16:23], v[190:197], v[76:79]
	v_mfma_f32_16x16x128_f8f6f4 v[68:71], v[182:189], v[190:197], v[68:71]
	v_mfma_f32_16x16x128_f8f6f4 v[60:63], v[16:23], v[206:213], v[60:63]
	v_mfma_f32_16x16x128_f8f6f4 v[52:55], v[182:189], v[206:213], v[52:55]
	v_mfma_f32_16x16x128_f8f6f4 v[44:47], v[16:23], v[214:221], v[44:47]
	v_mfma_f32_16x16x128_f8f6f4 v[36:39], v[182:189], v[214:221], v[36:39]
	v_mfma_f32_16x16x128_f8f6f4 v[28:31], v[16:23], v[222:229], v[28:31]
	v_mfma_f32_16x16x128_f8f6f4 v[24:27], v[182:189], v[222:229], v[24:27]
	s_setprio 0
	s_barrier
	s_add_i32 s59, 0, 0x18000
	s_add_i32 s60, 0, 0x1c000
	v_add_u32_e32 v0, s59, v180
	v_add_u32_e32 v20, s60, v180
	ds_read_b128 v[8:11], v0
	ds_read_b128 v[12:15], v0 offset:1024
	ds_read_b128 v[182:185], v0 offset:2048
	ds_read_b128 v[186:189], v0 offset:3072
	ds_read_b128 v[0:3], v20
	ds_read_b128 v[4:7], v20 offset:1024
	ds_read_b128 v[16:19], v20 offset:2048
	ds_read_b128 v[20:23], v20 offset:3072
	s_add_u32 s30, s30, 0x70000
	s_addc_u32 s31, s31, 0
	s_mov_b32 m0, s45
	v_lshl_add_u64 v[198:199], s[30:31], 0, v[158:159]
	ds_read_b128 v[190:193], v181 offset:32768
	ds_read_b128 v[194:197], v181 offset:33792
	ds_read_b128 v[206:209], v181 offset:34816
	ds_read_b128 v[210:213], v181 offset:35840
	ds_read_b128 v[214:217], v181 offset:36864
	ds_read_b128 v[218:221], v181 offset:37888
	ds_read_b128 v[222:225], v181 offset:38912
	ds_read_b128 v[226:229], v181 offset:39936
	global_load_lds_dwordx4 v[198:199], off
	v_lshl_add_u64 v[198:199], s[30:31], 0, v[154:155]
	s_mov_b32 m0, s46
	s_nop 0
	global_load_lds_dwordx4 v[198:199], off
	s_waitcnt vmcnt(8)
	s_waitcnt lgkmcnt(0)
	s_barrier
; #define PG8_STAGE(bufoff, gbase, voff) do { _Pragma("unroll") for (int _i = 0; _i < 2; ++_i) \
;         __builtin_amdgcn_global_load_lds((const unsigned*)((const char*)(gbase) + (voff)[_i]), (PG8_LAS unsigned*)(lds + (bufoff) + ldsw + _i * 8192), 16, 0, 0); } while (0)
; #define PG8_WAIT_V(n) asm volatile("s_waitcnt vmcnt(" #n ")" ::: "memory")
; #define PG8_WAIT_L(n) asm volatile("s_waitcnt lgkmcnt(" #n ")" ::: "memory")
; #define PG8_BAR __builtin_amdgcn_s_barrier()
; #define PG8_SCHED __builtin_amdgcn_sched_barrier(0)
; template <class Epi, class Sched, bool ALIGN_EPI = false, bool SP2 = false, bool FP8 = false, bool PEEL = false>
; __device__ __forceinline__ void gemm_phase(PG8_LAS unsigned char* lds, const Gemm g, const Sched& S, const Epi& E, const int wid) {
;     ...
;             const bool last = (t == nt - 2);
;     ...
;             PG8_LDA(At, 1, 1); PG8_STAGE(PG8_SB(1, 0), b3, voffB); PG8_STAGE(PG8_SB(1, 1), b3 + hstep, voffB); PG8_STAGE(PG8_SA(1, 0), a3, voffA);
;             PG8_WAIT_V(8); PG8_WAIT_L(0); PG8_BAR; PG8_MMA(1, 0, At, B0); PG8_MMA(1, 1, At, B1); PG8_BAR; PG8_SCHED;
	s_setprio 1
	s_waitcnt lgkmcnt(0)
	v_mfma_f32_16x16x128_f8f6f4 v[148:151], v[8:15], v[190:197], v[148:151]
	v_mfma_f32_16x16x128_f8f6f4 v[144:147], v[182:189], v[190:197], v[144:147]
	v_mfma_f32_16x16x128_f8f6f4 v[136:139], v[8:15], v[206:213], v[136:139]
	v_mfma_f32_16x16x128_f8f6f4 v[128:131], v[182:189], v[206:213], v[128:131]
	v_mfma_f32_16x16x128_f8f6f4 v[120:123], v[8:15], v[214:221], v[120:123]
	v_mfma_f32_16x16x128_f8f6f4 v[112:115], v[182:189], v[214:221], v[112:115]
	v_mfma_f32_16x16x128_f8f6f4 v[104:107], v[8:15], v[222:229], v[104:107]
	v_mfma_f32_16x16x128_f8f6f4 v[96:99], v[182:189], v[222:229], v[96:99]
	s_setprio 0
	s_setprio 1
	v_mfma_f32_16x16x128_f8f6f4 v[140:143], v[0:7], v[190:197], v[140:143]
	v_mfma_f32_16x16x128_f8f6f4 v[132:135], v[16:23], v[190:197], v[132:135]
	v_mfma_f32_16x16x128_f8f6f4 v[124:127], v[0:7], v[206:213], v[124:127]
	v_mfma_f32_16x16x128_f8f6f4 v[116:119], v[16:23], v[206:213], v[116:119]
	v_mfma_f32_16x16x128_f8f6f4 v[108:111], v[0:7], v[214:221], v[108:111]
	v_mfma_f32_16x16x128_f8f6f4 v[100:103], v[16:23], v[214:221], v[100:103]
	v_mfma_f32_16x16x128_f8f6f4 v[92:95], v[0:7], v[222:229], v[92:95]
	v_mfma_f32_16x16x128_f8f6f4 v[88:91], v[16:23], v[222:229], v[88:91]
	s_setprio 0
	s_barrier
	s_add_i32 s30, s59, s40
	v_lshl_add_u64 v[172:173], v[172:173], 0, s[14:15]
	s_mov_b32 m0, s30
	ds_read_b128 v[190:193], v181 offset:49152
	ds_read_b128 v[194:197], v181 offset:50176
	ds_read_b128 v[206:209], v181 offset:51200
	ds_read_b128 v[210:213], v181 offset:52224
	ds_read_b128 v[214:217], v181 offset:53248
	ds_read_b128 v[218:221], v181 offset:54272
	ds_read_b128 v[222:225], v181 offset:55296
	ds_read_b128 v[226:229], v181 offset:56320
	global_load_lds_dwordx4 v[172:173], off
	s_add_i32 m0, s30, 0x2000
	s_add_u32 s26, s26, 0x70080
	v_lshl_add_u64 v[172:173], v[174:175], 0, s[14:15]
	s_addc_u32 s27, s27, 0
	s_add_i32 s30, s60, s40
	global_load_lds_dwordx4 v[172:173], off
	v_lshl_add_u64 v[172:173], s[26:27], 0, v[156:157]
	s_mov_b32 m0, s30
	s_nop 0
	global_load_lds_dwordx4 v[172:173], off
	v_lshl_add_u64 v[172:173], s[26:27], 0, v[152:153]
	s_add_i32 m0, s30, 0x2000
	s_nop 0
	global_load_lds_dwordx4 v[172:173], off
	v_lshl_add_u64 v[172:173], v[176:177], 0, s[14:15]
	s_mov_b32 m0, s47
	s_nop 0
	global_load_lds_dwordx4 v[172:173], off
	v_lshl_add_u64 v[172:173], v[178:179], 0, s[14:15]
	s_mov_b32 m0, s48
	s_nop 0
	global_load_lds_dwordx4 v[172:173], off
	s_waitcnt vmcnt(8)
	s_waitcnt lgkmcnt(0)
	s_barrier
	s_setprio 1
	s_waitcnt lgkmcnt(0)
	v_mfma_f32_16x16x128_f8f6f4 v[84:87], v[8:15], v[190:197], v[84:87]
	v_mfma_f32_16x16x128_f8f6f4 v[80:83], v[182:189], v[190:197], v[80:83]
	v_mfma_f32_16x16x128_f8f6f4 v[72:75], v[8:15], v[206:213], v[72:75]
	v_mfma_f32_16x16x128_f8f6f4 v[64:67], v[182:189], v[206:213], v[64:67]
	v_mfma_f32_16x16x128_f8f6f4 v[56:59], v[8:15], v[214:221], v[56:59]
	v_mfma_f32_16x16x128_f8f6f4 v[48:51], v[182:189], v[214:221], v[48:51]
	v_mfma_f32_16x16x128_f8f6f4 v[40:43], v[8:15], v[222:229], v[40:43]
	v_mfma_f32_16x16x128_f8f6f4 v[32:35], v[182:189], v[222:229], v[32:35]
	s_setprio 0
	s_setprio 1
	v_mfma_f32_16x16x128_f8f6f4 v[76:79], v[0:7], v[190:197], v[76:79]
	v_mfma_f32_16x16x128_f8f6f4 v[68:71], v[16:23], v[190:197], v[68:71]
	v_mfma_f32_16x16x128_f8f6f4 v[60:63], v[0:7], v[206:213], v[60:63]
	v_mfma_f32_16x16x128_f8f6f4 v[52:55], v[16:23], v[206:213], v[52:55]
	v_mfma_f32_16x16x128_f8f6f4 v[44:47], v[0:7], v[214:221], v[44:47]
	v_mfma_f32_16x16x128_f8f6f4 v[36:39], v[16:23], v[214:221], v[36:39]
	v_mfma_f32_16x16x128_f8f6f4 v[28:31], v[0:7], v[222:229], v[28:31]
	v_mfma_f32_16x16x128_f8f6f4 v[24:27], v[16:23], v[222:229], v[24:27]
	s_add_i32 s58, s58, 2
	s_add_u32 s24, s24, 0x100
	s_addc_u32 s25, s25, 0
	s_cmp_gt_u32 s58, 25
	s_setprio 0
	s_barrier
; template <class Epi, class Sched, bool ALIGN_EPI = false, bool SP2 = false, bool FP8 = false, bool PEEL = false>
; __device__ __forceinline__ void gemm_phase(PG8_LAS unsigned char* lds, const Gemm g, const Sched& S, const Epi& E, const int wid) {
;     ...
;         if constexpr (FP8) asm volatile("s_nop 15\n\ts_nop 15" ::: "memory");
;         if constexpr (!Epi::AFTER_DRAIN) { E(acc, cur, wr, wc, fr, fq); S.done(cur); }
;         if (!has_next) break;
;         if constexpr (!PEEL) {
; #pragma unroll
;         for (int a = 0; a < 2; ++a)
; #pragma unroll
;             for (int b = 0; b < 2; ++b)
; #pragma unroll
;                 for (int m = 0; m < 4; ++m)
; #pragma unroll
;                     for (int n = 0; n < 2; ++n) acc[a][b][m][n] = (f32x4){0.f, 0.f, 0.f, 0.f};
	s_cbranch_scc0 .LBB0_976
	s_nop 15
	s_nop 15
	s_add_u32 s24, s56, 0xffffff00
	s_addc_u32 s25, s57, -1
	s_and_b64 vcc, exec, s[10:11]
	s_cbranch_vccnz .LBB0_979
	v_mov_b32_e32 v24, 0
	s_mov_b32 s4, s52
	s_mov_b32 s3, s53
	s_mov_b64 s[6:7], s[16:17]
	s_mov_b32 s49, s55
	v_mov_b32_e32 v25, v24
	v_mov_b32_e32 v26, v24
	v_mov_b32_e32 v27, v24
	v_mov_b32_e32 v28, v24
	v_mov_b32_e32 v29, v24
	v_mov_b32_e32 v30, v24
	v_mov_b32_e32 v31, v24
	v_mov_b32_e32 v36, v24
	v_mov_b32_e32 v37, v24
	v_mov_b32_e32 v38, v24
	v_mov_b32_e32 v39, v24
	v_mov_b32_e32 v44, v24
	v_mov_b32_e32 v45, v24
	v_mov_b32_e32 v46, v24
	v_mov_b32_e32 v47, v24
	v_mov_b32_e32 v52, v24
	v_mov_b32_e32 v53, v24
	v_mov_b32_e32 v54, v24
	v_mov_b32_e32 v55, v24
	v_mov_b32_e32 v60, v24
	v_mov_b32_e32 v61, v24
	v_mov_b32_e32 v62, v24
	v_mov_b32_e32 v63, v24
	v_mov_b32_e32 v68, v24
	v_mov_b32_e32 v69, v24
	v_mov_b32_e32 v70, v24
	v_mov_b32_e32 v71, v24
	v_mov_b32_e32 v76, v24
	v_mov_b32_e32 v77, v24
	v_mov_b32_e32 v78, v24
	v_mov_b32_e32 v79, v24
	v_mov_b32_e32 v32, v24
	v_mov_b32_e32 v33, v24
	v_mov_b32_e32 v34, v24
	v_mov_b32_e32 v35, v24
	v_mov_b32_e32 v40, v24
	v_mov_b32_e32 v41, v24
	v_mov_b32_e32 v42, v24
	v_mov_b32_e32 v43, v24
	v_mov_b32_e32 v48, v24
	v_mov_b32_e32 v49, v24
	v_mov_b32_e32 v50, v24
	v_mov_b32_e32 v51, v24
	v_mov_b32_e32 v56, v24
	v_mov_b32_e32 v57, v24
	v_mov_b32_e32 v58, v24
	v_mov_b32_e32 v59, v24
	v_mov_b32_e32 v64, v24
	v_mov_b32_e32 v65, v24
	v_mov_b32_e32 v66, v24
	v_mov_b32_e32 v67, v24
	v_mov_b32_e32 v72, v24
	v_mov_b32_e32 v73, v24
	v_mov_b32_e32 v74, v24
	v_mov_b32_e32 v75, v24
	v_mov_b32_e32 v80, v24
	v_mov_b32_e32 v81, v24
	v_mov_b32_e32 v82, v24
	v_mov_b32_e32 v83, v24
	v_mov_b32_e32 v84, v24
	v_mov_b32_e32 v85, v24
	v_mov_b32_e32 v86, v24
	v_mov_b32_e32 v87, v24
	v_mov_b32_e32 v88, v24
	v_mov_b32_e32 v89, v24
	v_mov_b32_e32 v90, v24
	v_mov_b32_e32 v91, v24
	v_mov_b32_e32 v92, v24
	v_mov_b32_e32 v93, v24
	v_mov_b32_e32 v94, v24
	v_mov_b32_e32 v95, v24
	v_mov_b32_e32 v100, v24
	v_mov_b32_e32 v101, v24
	v_mov_b32_e32 v102, v24
	v_mov_b32_e32 v103, v24
	v_mov_b32_e32 v108, v24
	v_mov_b32_e32 v109, v24
	v_mov_b32_e32 v110, v24
	v_mov_b32_e32 v111, v24
	v_mov_b32_e32 v116, v24
	v_mov_b32_e32 v117, v24
	v_mov_b32_e32 v118, v24
	v_mov_b32_e32 v119, v24
	v_mov_b32_e32 v124, v24
	v_mov_b32_e32 v125, v24
	v_mov_b32_e32 v126, v24
	v_mov_b32_e32 v127, v24
	v_mov_b32_e32 v132, v24
	v_mov_b32_e32 v133, v24
	v_mov_b32_e32 v134, v24
	v_mov_b32_e32 v135, v24
	v_mov_b32_e32 v140, v24
	v_mov_b32_e32 v141, v24
	v_mov_b32_e32 v142, v24
	v_mov_b32_e32 v143, v24
	v_mov_b32_e32 v96, v24
	v_mov_b32_e32 v97, v24
	v_mov_b32_e32 v98, v24
	v_mov_b32_e32 v99, v24
	v_mov_b32_e32 v104, v24
	v_mov_b32_e32 v105, v24
	v_mov_b32_e32 v106, v24
	v_mov_b32_e32 v107, v24
	v_mov_b32_e32 v112, v24
	v_mov_b32_e32 v113, v24
	v_mov_b32_e32 v114, v24
	v_mov_b32_e32 v115, v24
	v_mov_b32_e32 v120, v24
	v_mov_b32_e32 v121, v24
	v_mov_b32_e32 v122, v24
	v_mov_b32_e32 v123, v24
	v_mov_b32_e32 v128, v24
	v_mov_b32_e32 v129, v24
	v_mov_b32_e32 v130, v24
	v_mov_b32_e32 v131, v24
	v_mov_b32_e32 v136, v24
	v_mov_b32_e32 v137, v24
	v_mov_b32_e32 v138, v24
	v_mov_b32_e32 v139, v24
	v_mov_b32_e32 v144, v24
	v_mov_b32_e32 v145, v24
	v_mov_b32_e32 v146, v24
	v_mov_b32_e32 v147, v24
	v_mov_b32_e32 v148, v24
	v_mov_b32_e32 v149, v24
	v_mov_b32_e32 v150, v24
	v_mov_b32_e32 v151, v24
	s_andn2_b64 vcc, exec, s[8:9]
	s_cbranch_vccnz .LBB0_980
	s_branch .LBB0_981

; #define PG8_STAGE(bufoff, gbase, voff) do { _Pragma("unroll") for (int _i = 0; _i < 2; ++_i) \
;         __builtin_amdgcn_global_load_lds((const unsigned*)((const char*)(gbase) + (voff)[_i]), (PG8_LAS unsigned*)(lds + (bufoff) + ldsw + _i * 8192), 16, 0, 0); } while (0)
; #define PG8_WAIT_V(n) asm volatile("s_waitcnt vmcnt(" #n ")" ::: "memory")
; #define PG8_WAIT_L(n) asm volatile("s_waitcnt lgkmcnt(" #n ")" ::: "memory")
; #define PG8_BAR __builtin_amdgcn_s_barrier()
; #define PG8_SCHED __builtin_amdgcn_sched_barrier(0)
; template <class Epi, class Sched, bool ALIGN_EPI = false, bool SP2 = false, bool FP8 = false, bool PEEL = false>
; __device__ __forceinline__ void gemm_phase(PG8_LAS unsigned char* lds, const Gemm g, const Sched& S, const Epi& E, const int wid) {
;     ...
;             const bool last = (t == nt - 2);
;             const char* a1 = cA + (size_t)(t + 1) * kstep;
;             const char* a2 = last ? nA : cA + (size_t)(t + 2) * kstep; const char* b2 = last ? nB : cB + (size_t)(t + 2) * kstep;
;             const char* a3 = a2 + kstep; const char* b3 = b2 + kstep;
;             if (last && has_next) S.a_ready(nxt);
;             PG8_LDB(B0, 0, 0); PG8_LDB(B1, 0, 1); PG8_SCHED; PG8_LDA(At, 0, 0); PG8_STAGE(PG8_SA(1, 1), a1 + hstep, voffA);
;             PG8_WAIT_V(8); PG8_WAIT_L(0); PG8_BAR; PG8_MMA(0, 0, At, B0); PG8_MMA(0, 1, At, B1); PG8_BAR; PG8_SCHED;
.LBB0_1120:
	ds_read_b128 v[146:149], v152
	ds_read_b128 v[156:159], v152 offset:1024
	ds_read_b128 v[160:163], v152 offset:2048
	ds_read_b128 v[164:167], v152 offset:3072
	ds_read_b128 v[168:171], v153
	ds_read_b128 v[172:175], v153 offset:1024
	ds_read_b128 v[176:179], v153 offset:2048
	ds_read_b128 v[180:183], v153 offset:3072
	s_add_u32 s44, s36, 0xfffc0080
	s_addc_u32 s45, s37, -1
	s_cmp_eq_u32 s61, 12
	s_cselect_b32 s47, s10, s45
	s_cselect_b32 s46, s25, s44
	s_cselect_b32 s45, s17, s60
	s_cselect_b32 s44, s58, s59
	v_lshl_add_u64 v[216:217], s[36:37], 0, v[136:137]
	s_add_i32 m0, s41, 0xc000
	ds_read_b128 v[184:187], v154
	ds_read_b128 v[188:191], v154 offset:1024
	ds_read_b128 v[192:195], v154 offset:2048
	ds_read_b128 v[196:199], v154 offset:3072
	ds_read_b128 v[200:203], v154 offset:4096
	ds_read_b128 v[204:207], v154 offset:5120
	ds_read_b128 v[208:211], v154 offset:6144
	ds_read_b128 v[212:215], v154 offset:7168
	global_load_lds_dwordx4 v[216:217], off
	v_lshl_add_u64 v[216:217], s[36:37], 0, v[138:139]
	s_add_i32 m0, s41, 0xe000
	s_nop 0
	global_load_lds_dwordx4 v[216:217], off
	s_waitcnt vmcnt(8)
	s_waitcnt lgkmcnt(0)
	s_barrier
	s_setprio 1
	s_waitcnt lgkmcnt(0)
	v_mfma_f32_16x16x32_bf16 v[124:127], v[146:149], v[184:187], v[124:127]
	v_mfma_f32_16x16x32_bf16 v[120:123], v[160:163], v[184:187], v[120:123]
	v_mfma_f32_16x16x32_bf16 v[112:115], v[146:149], v[192:195], v[112:115]
	v_mfma_f32_16x16x32_bf16 v[104:107], v[160:163], v[192:195], v[104:107]
	v_mfma_f32_16x16x32_bf16 v[96:99], v[146:149], v[200:203], v[96:99]
	v_mfma_f32_16x16x32_bf16 v[88:91], v[160:163], v[200:203], v[88:91]
	v_mfma_f32_16x16x32_bf16 v[80:83], v[146:149], v[208:211], v[80:83]
	v_mfma_f32_16x16x32_bf16 v[72:75], v[160:163], v[208:211], v[72:75]
	v_mfma_f32_16x16x32_bf16 v[124:127], v[156:159], v[188:191], v[124:127]
	v_mfma_f32_16x16x32_bf16 v[120:123], v[164:167], v[188:191], v[120:123]
	v_mfma_f32_16x16x32_bf16 v[112:115], v[156:159], v[196:199], v[112:115]
	v_mfma_f32_16x16x32_bf16 v[104:107], v[164:167], v[196:199], v[104:107]
	v_mfma_f32_16x16x32_bf16 v[96:99], v[156:159], v[204:207], v[96:99]
	v_mfma_f32_16x16x32_bf16 v[88:91], v[164:167], v[204:207], v[88:91]
	v_mfma_f32_16x16x32_bf16 v[80:83], v[156:159], v[212:215], v[80:83]
	v_mfma_f32_16x16x32_bf16 v[72:75], v[164:167], v[212:215], v[72:75]
	s_setprio 0
	s_setprio 1
	v_mfma_f32_16x16x32_bf16 v[116:119], v[168:171], v[184:187], v[116:119]
	v_mfma_f32_16x16x32_bf16 v[108:111], v[176:179], v[184:187], v[108:111]
	v_mfma_f32_16x16x32_bf16 v[100:103], v[168:171], v[192:195], v[100:103]
	v_mfma_f32_16x16x32_bf16 v[92:95], v[176:179], v[192:195], v[92:95]
	v_mfma_f32_16x16x32_bf16 v[84:87], v[168:171], v[200:203], v[84:87]
	v_mfma_f32_16x16x32_bf16 v[76:79], v[176:179], v[200:203], v[76:79]
	v_mfma_f32_16x16x32_bf16 v[68:71], v[168:171], v[208:211], v[68:71]
	v_mfma_f32_16x16x32_bf16 v[64:67], v[176:179], v[208:211], v[64:67]
	v_mfma_f32_16x16x32_bf16 v[116:119], v[172:175], v[188:191], v[116:119]
	v_mfma_f32_16x16x32_bf16 v[108:111], v[180:183], v[188:191], v[108:111]
	v_mfma_f32_16x16x32_bf16 v[100:103], v[172:175], v[196:199], v[100:103]
	v_mfma_f32_16x16x32_bf16 v[92:95], v[180:183], v[196:199], v[92:95]
	v_mfma_f32_16x16x32_bf16 v[84:87], v[172:175], v[204:207], v[84:87]
	v_mfma_f32_16x16x32_bf16 v[76:79], v[180:183], v[204:207], v[76:79]
	v_mfma_f32_16x16x32_bf16 v[68:71], v[172:175], v[212:215], v[68:71]
	v_mfma_f32_16x16x32_bf16 v[64:67], v[180:183], v[212:215], v[64:67]
	s_setprio 0
	s_barrier
	s_add_i32 s62, s52, s3
	v_lshl_add_u64 v[216:217], s[44:45], 0, v[132:133]
	s_mov_b32 m0, s62
	ds_read_b128 v[184:187], v154 offset:16384
	ds_read_b128 v[188:191], v154 offset:17408
	ds_read_b128 v[192:195], v154 offset:18432
	ds_read_b128 v[196:199], v154 offset:19456
	ds_read_b128 v[200:203], v154 offset:20480
	ds_read_b128 v[204:207], v154 offset:21504
	ds_read_b128 v[208:211], v154 offset:22528
	ds_read_b128 v[212:215], v154 offset:23552
	global_load_lds_dwordx4 v[216:217], off
	s_add_i32 m0, s62, 0x2000
	s_add_u32 s62, s44, 0x40000
	v_lshl_add_u64 v[218:219], s[44:45], 0, v[128:129]
	s_addc_u32 s63, s45, 0
	s_add_i32 s64, s53, s3
	global_load_lds_dwordx4 v[218:219], off
	v_lshl_add_u64 v[220:221], s[62:63], 0, v[132:133]
	s_mov_b32 m0, s64
	v_lshl_add_u64 v[222:223], s[46:47], 0, v[130:131]
	global_load_lds_dwordx4 v[220:221], off
	v_lshl_add_u64 v[220:221], s[62:63], 0, v[128:129]
	s_add_i32 m0, s64, 0x2000
	s_nop 0
	global_load_lds_dwordx4 v[220:221], off
	v_lshl_add_u64 v[220:221], s[46:47], 0, v[134:135]
	s_mov_b32 m0, s41
	s_nop 0
	global_load_lds_dwordx4 v[220:221], off
	s_mov_b32 m0, s42
	s_nop 0
	global_load_lds_dwordx4 v[222:223], off
	s_waitcnt vmcnt(8)
	s_waitcnt lgkmcnt(0)
	s_barrier
; #define PG8_STAGE(bufoff, gbase, voff) do { _Pragma("unroll") for (int _i = 0; _i < 2; ++_i) \
;         __builtin_amdgcn_global_load_lds((const unsigned*)((const char*)(gbase) + (voff)[_i]), (PG8_LAS unsigned*)(lds + (bufoff) + ldsw + _i * 8192), 16, 0, 0); } while (0)
; #define PG8_WAIT_V(n) asm volatile("s_waitcnt vmcnt(" #n ")" ::: "memory")
; #define PG8_WAIT_L(n) asm volatile("s_waitcnt lgkmcnt(" #n ")" ::: "memory")
; #define PG8_BAR __builtin_amdgcn_s_barrier()
; #define PG8_SCHED __builtin_amdgcn_sched_barrier(0)
; template <class Epi, class Sched, bool ALIGN_EPI = false, bool SP2 = false, bool FP8 = false, bool PEEL = false>
; __device__ __forceinline__ void gemm_phase(PG8_LAS unsigned char* lds, const Gemm g, const Sched& S, const Epi& E, const int wid) {
;     ...
;             PG8_WAIT_V(8); PG8_WAIT_L(0); PG8_BAR; PG8_MMA(0, 0, At, B0); PG8_MMA(0, 1, At, B1); PG8_BAR; PG8_SCHED;
;             PG8_LDA(At, 0, 1); PG8_STAGE(PG8_SB(0, 0), b2, voffB); PG8_STAGE(PG8_SB(0, 1), b2 + hstep, voffB); PG8_STAGE(PG8_SA(0, 0), a2, voffA);
;             PG8_WAIT_V(8); PG8_WAIT_L(0); PG8_BAR; PG8_MMA(1, 0, At, B0); PG8_MMA(1, 1, At, B1); PG8_BAR; PG8_SCHED;
;             PG8_LDB(B0, 1, 0); PG8_LDB(B1, 1, 1); PG8_SCHED; PG8_LDA(At, 1, 0); PG8_STAGE(PG8_SA(0, 1), a2 + hstep, voffA);
;             PG8_WAIT_V(8); PG8_WAIT_L(0); PG8_BAR; PG8_MMA(0, 0, At, B0); PG8_MMA(0, 1, At, B1); PG8_BAR; PG8_SCHED;
;             PG8_LDA(At, 1, 1); PG8_STAGE(PG8_SB(1, 0), b3, voffB); PG8_STAGE(PG8_SB(1, 1), b3 + hstep, voffB); PG8_STAGE(PG8_SA(1, 0), a3, voffA);
	s_setprio 1
	s_waitcnt lgkmcnt(0)
	v_mfma_f32_16x16x32_bf16 v[60:63], v[146:149], v[184:187], v[60:63]
	v_mfma_f32_16x16x32_bf16 v[56:59], v[160:163], v[184:187], v[56:59]
	v_mfma_f32_16x16x32_bf16 v[48:51], v[146:149], v[192:195], v[48:51]
	v_mfma_f32_16x16x32_bf16 v[40:43], v[160:163], v[192:195], v[40:43]
	v_mfma_f32_16x16x32_bf16 v[32:35], v[146:149], v[200:203], v[32:35]
	v_mfma_f32_16x16x32_bf16 v[24:27], v[160:163], v[200:203], v[24:27]
	v_mfma_f32_16x16x32_bf16 v[16:19], v[146:149], v[208:211], v[16:19]
	v_mfma_f32_16x16x32_bf16 v[8:11], v[160:163], v[208:211], v[8:11]
	v_mfma_f32_16x16x32_bf16 v[60:63], v[156:159], v[188:191], v[60:63]
	v_mfma_f32_16x16x32_bf16 v[56:59], v[164:167], v[188:191], v[56:59]
	v_mfma_f32_16x16x32_bf16 v[48:51], v[156:159], v[196:199], v[48:51]
	v_mfma_f32_16x16x32_bf16 v[40:43], v[164:167], v[196:199], v[40:43]
	v_mfma_f32_16x16x32_bf16 v[32:35], v[156:159], v[204:207], v[32:35]
	v_mfma_f32_16x16x32_bf16 v[24:27], v[164:167], v[204:207], v[24:27]
	v_mfma_f32_16x16x32_bf16 v[16:19], v[156:159], v[212:215], v[16:19]
	v_mfma_f32_16x16x32_bf16 v[8:11], v[164:167], v[212:215], v[8:11]
	s_setprio 0
	s_setprio 1
	v_mfma_f32_16x16x32_bf16 v[52:55], v[168:171], v[184:187], v[52:55]
	v_mfma_f32_16x16x32_bf16 v[44:47], v[176:179], v[184:187], v[44:47]
	v_mfma_f32_16x16x32_bf16 v[36:39], v[168:171], v[192:195], v[36:39]
	v_mfma_f32_16x16x32_bf16 v[28:31], v[176:179], v[192:195], v[28:31]
	v_mfma_f32_16x16x32_bf16 v[20:23], v[168:171], v[200:203], v[20:23]
	v_mfma_f32_16x16x32_bf16 v[12:15], v[176:179], v[200:203], v[12:15]
	v_mfma_f32_16x16x32_bf16 v[4:7], v[168:171], v[208:211], v[4:7]
	v_mfma_f32_16x16x32_bf16 v[0:3], v[176:179], v[208:211], v[0:3]
	v_mfma_f32_16x16x32_bf16 v[52:55], v[172:175], v[188:191], v[52:55]
	v_mfma_f32_16x16x32_bf16 v[44:47], v[180:183], v[188:191], v[44:47]
	v_mfma_f32_16x16x32_bf16 v[36:39], v[172:175], v[196:199], v[36:39]
	v_mfma_f32_16x16x32_bf16 v[28:31], v[180:183], v[196:199], v[28:31]
	v_mfma_f32_16x16x32_bf16 v[20:23], v[172:175], v[204:207], v[20:23]
	v_mfma_f32_16x16x32_bf16 v[12:15], v[180:183], v[204:207], v[12:15]
	v_mfma_f32_16x16x32_bf16 v[4:7], v[172:175], v[212:215], v[4:7]
	v_mfma_f32_16x16x32_bf16 v[0:3], v[180:183], v[212:215], v[0:3]
	s_setprio 0
	s_barrier
	s_add_i32 s62, 0, 0x18000
	v_add_u32_e32 v144, s62, v150
	s_add_i32 s63, 0, 0x1c000
	ds_read_b128 v[146:149], v144
	ds_read_b128 v[156:159], v144 offset:1024
	ds_read_b128 v[160:163], v144 offset:2048
	ds_read_b128 v[164:167], v144 offset:3072
	v_add_u32_e32 v144, s63, v150
	ds_read_b128 v[168:171], v144
	ds_read_b128 v[172:175], v144 offset:1024
	ds_read_b128 v[176:179], v144 offset:2048
	ds_read_b128 v[180:183], v144 offset:3072
	s_add_u32 s46, s46, 0x40000
	s_addc_u32 s47, s47, 0
	s_mov_b32 m0, s43
	v_lshl_add_u64 v[224:225], s[46:47], 0, v[134:135]
	ds_read_b128 v[184:187], v154 offset:32768
	ds_read_b128 v[188:191], v154 offset:33792
	ds_read_b128 v[192:195], v154 offset:34816
	ds_read_b128 v[196:199], v154 offset:35840
	ds_read_b128 v[200:203], v154 offset:36864
	ds_read_b128 v[204:207], v154 offset:37888
	ds_read_b128 v[208:211], v154 offset:38912
	ds_read_b128 v[212:215], v154 offset:39936
	global_load_lds_dwordx4 v[224:225], off
	v_lshl_add_u64 v[224:225], s[46:47], 0, v[130:131]
	s_mov_b32 m0, s48
	s_nop 0
	global_load_lds_dwordx4 v[224:225], off
	s_waitcnt vmcnt(8)
	s_waitcnt lgkmcnt(0)
	s_barrier
	s_setprio 1
	s_waitcnt lgkmcnt(0)
	v_mfma_f32_16x16x32_bf16 v[124:127], v[146:149], v[184:187], v[124:127]
	v_mfma_f32_16x16x32_bf16 v[120:123], v[160:163], v[184:187], v[120:123]
	v_mfma_f32_16x16x32_bf16 v[112:115], v[146:149], v[192:195], v[112:115]
	v_mfma_f32_16x16x32_bf16 v[104:107], v[160:163], v[192:195], v[104:107]
	v_mfma_f32_16x16x32_bf16 v[96:99], v[146:149], v[200:203], v[96:99]
	v_mfma_f32_16x16x32_bf16 v[88:91], v[160:163], v[200:203], v[88:91]
	v_mfma_f32_16x16x32_bf16 v[80:83], v[146:149], v[208:211], v[80:83]
	v_mfma_f32_16x16x32_bf16 v[72:75], v[160:163], v[208:211], v[72:75]
	v_mfma_f32_16x16x32_bf16 v[124:127], v[156:159], v[188:191], v[124:127]
	v_mfma_f32_16x16x32_bf16 v[120:123], v[164:167], v[188:191], v[120:123]
	v_mfma_f32_16x16x32_bf16 v[112:115], v[156:159], v[196:199], v[112:115]
	v_mfma_f32_16x16x32_bf16 v[104:107], v[164:167], v[196:199], v[104:107]
	v_mfma_f32_16x16x32_bf16 v[96:99], v[156:159], v[204:207], v[96:99]
	v_mfma_f32_16x16x32_bf16 v[88:91], v[164:167], v[204:207], v[88:91]
	v_mfma_f32_16x16x32_bf16 v[80:83], v[156:159], v[212:215], v[80:83]
	v_mfma_f32_16x16x32_bf16 v[72:75], v[164:167], v[212:215], v[72:75]
	s_setprio 0
	s_setprio 1
	v_mfma_f32_16x16x32_bf16 v[116:119], v[168:171], v[184:187], v[116:119]
	v_mfma_f32_16x16x32_bf16 v[108:111], v[176:179], v[184:187], v[108:111]
	v_mfma_f32_16x16x32_bf16 v[100:103], v[168:171], v[192:195], v[100:103]
	v_mfma_f32_16x16x32_bf16 v[92:95], v[176:179], v[192:195], v[92:95]
	v_mfma_f32_16x16x32_bf16 v[84:87], v[168:171], v[200:203], v[84:87]
	v_mfma_f32_16x16x32_bf16 v[76:79], v[176:179], v[200:203], v[76:79]
	v_mfma_f32_16x16x32_bf16 v[68:71], v[168:171], v[208:211], v[68:71]
	v_mfma_f32_16x16x32_bf16 v[64:67], v[176:179], v[208:211], v[64:67]
	v_mfma_f32_16x16x32_bf16 v[116:119], v[172:175], v[188:191], v[116:119]
	v_mfma_f32_16x16x32_bf16 v[108:111], v[180:183], v[188:191], v[108:111]
	v_mfma_f32_16x16x32_bf16 v[100:103], v[172:175], v[196:199], v[100:103]
	v_mfma_f32_16x16x32_bf16 v[92:95], v[180:183], v[196:199], v[92:95]
	v_mfma_f32_16x16x32_bf16 v[84:87], v[172:175], v[204:207], v[84:87]
	v_mfma_f32_16x16x32_bf16 v[76:79], v[180:183], v[204:207], v[76:79]
	v_mfma_f32_16x16x32_bf16 v[68:71], v[172:175], v[212:215], v[68:71]
	v_mfma_f32_16x16x32_bf16 v[64:67], v[180:183], v[212:215], v[64:67]
	s_setprio 0
	s_barrier
; #define PG8_STAGE(bufoff, gbase, voff) do { _Pragma("unroll") for (int _i = 0; _i < 2; ++_i) \
;         __builtin_amdgcn_global_load_lds((const unsigned*)((const char*)(gbase) + (voff)[_i]), (PG8_LAS unsigned*)(lds + (bufoff) + ldsw + _i * 8192), 16, 0, 0); } while (0)
; #define PG8_WAIT_V(n) asm volatile("s_waitcnt vmcnt(" #n ")" ::: "memory")
; #define PG8_WAIT_L(n) asm volatile("s_waitcnt lgkmcnt(" #n ")" ::: "memory")
; #define PG8_BAR __builtin_amdgcn_s_barrier()
; #define PG8_SCHED __builtin_amdgcn_sched_barrier(0)
; template <class Epi, class Sched, bool ALIGN_EPI = false, bool SP2 = false, bool FP8 = false, bool PEEL = false>
; __device__ __forceinline__ void gemm_phase(PG8_LAS unsigned char* lds, const Gemm g, const Sched& S, const Epi& E, const int wid) {
;     ...
;         for (int t = 2; t < nt; t += 2) {
;     ...
;             PG8_LDA(At, 1, 1); PG8_STAGE(PG8_SB(1, 0), b3, voffB); PG8_STAGE(PG8_SB(1, 1), b3 + hstep, voffB); PG8_STAGE(PG8_SA(1, 0), a3, voffA);
;             PG8_WAIT_V(8); PG8_WAIT_L(0); PG8_BAR; PG8_MMA(1, 0, At, B0); PG8_MMA(1, 1, At, B1); PG8_BAR; PG8_SCHED;
	s_add_i32 s46, s62, s3
	v_lshl_add_u64 v[216:217], v[216:217], 0, s[14:15]
	s_mov_b32 m0, s46
	ds_read_b128 v[184:187], v154 offset:49152
	ds_read_b128 v[188:191], v154 offset:50176
	ds_read_b128 v[192:195], v154 offset:51200
	ds_read_b128 v[196:199], v154 offset:52224
	ds_read_b128 v[200:203], v154 offset:53248
	ds_read_b128 v[204:207], v154 offset:54272
	ds_read_b128 v[208:211], v154 offset:55296
	ds_read_b128 v[212:215], v154 offset:56320
	global_load_lds_dwordx4 v[216:217], off
	s_add_i32 m0, s46, 0x2000
	s_add_u32 s44, s44, 0x40080
	v_lshl_add_u64 v[216:217], v[218:219], 0, s[14:15]
	s_addc_u32 s45, s45, 0
	s_add_i32 s46, s63, s3
	global_load_lds_dwordx4 v[216:217], off
	v_lshl_add_u64 v[216:217], s[44:45], 0, v[132:133]
	s_mov_b32 m0, s46
	s_nop 0
	global_load_lds_dwordx4 v[216:217], off
	v_lshl_add_u64 v[216:217], s[44:45], 0, v[128:129]
	s_add_i32 m0, s46, 0x2000
	s_nop 0
	global_load_lds_dwordx4 v[216:217], off
	v_lshl_add_u64 v[216:217], v[220:221], 0, s[14:15]
	s_mov_b32 m0, s50
	s_nop 0
	global_load_lds_dwordx4 v[216:217], off
	v_lshl_add_u64 v[216:217], v[222:223], 0, s[14:15]
	s_mov_b32 m0, s51
	s_nop 0
	global_load_lds_dwordx4 v[216:217], off
	s_waitcnt vmcnt(8)
	s_waitcnt lgkmcnt(0)
	s_barrier
	s_setprio 1
	s_waitcnt lgkmcnt(0)
	v_mfma_f32_16x16x32_bf16 v[60:63], v[146:149], v[184:187], v[60:63]
	v_mfma_f32_16x16x32_bf16 v[56:59], v[160:163], v[184:187], v[56:59]
	v_mfma_f32_16x16x32_bf16 v[48:51], v[146:149], v[192:195], v[48:51]
	v_mfma_f32_16x16x32_bf16 v[40:43], v[160:163], v[192:195], v[40:43]
	v_mfma_f32_16x16x32_bf16 v[32:35], v[146:149], v[200:203], v[32:35]
	v_mfma_f32_16x16x32_bf16 v[24:27], v[160:163], v[200:203], v[24:27]
	v_mfma_f32_16x16x32_bf16 v[16:19], v[146:149], v[208:211], v[16:19]
	v_mfma_f32_16x16x32_bf16 v[8:11], v[160:163], v[208:211], v[8:11]
	v_mfma_f32_16x16x32_bf16 v[60:63], v[156:159], v[188:191], v[60:63]
	v_mfma_f32_16x16x32_bf16 v[56:59], v[164:167], v[188:191], v[56:59]
	v_mfma_f32_16x16x32_bf16 v[48:51], v[156:159], v[196:199], v[48:51]
	v_mfma_f32_16x16x32_bf16 v[40:43], v[164:167], v[196:199], v[40:43]
	v_mfma_f32_16x16x32_bf16 v[32:35], v[156:159], v[204:207], v[32:35]
	v_mfma_f32_16x16x32_bf16 v[24:27], v[164:167], v[204:207], v[24:27]
	v_mfma_f32_16x16x32_bf16 v[16:19], v[156:159], v[212:215], v[16:19]
	v_mfma_f32_16x16x32_bf16 v[8:11], v[164:167], v[212:215], v[8:11]
	s_setprio 0
	s_setprio 1
	v_mfma_f32_16x16x32_bf16 v[52:55], v[168:171], v[184:187], v[52:55]
	v_mfma_f32_16x16x32_bf16 v[44:47], v[176:179], v[184:187], v[44:47]
	v_mfma_f32_16x16x32_bf16 v[36:39], v[168:171], v[192:195], v[36:39]
	v_mfma_f32_16x16x32_bf16 v[28:31], v[176:179], v[192:195], v[28:31]
	v_mfma_f32_16x16x32_bf16 v[20:23], v[168:171], v[200:203], v[20:23]
	v_mfma_f32_16x16x32_bf16 v[12:15], v[176:179], v[200:203], v[12:15]
	v_mfma_f32_16x16x32_bf16 v[4:7], v[168:171], v[208:211], v[4:7]
	v_mfma_f32_16x16x32_bf16 v[0:3], v[176:179], v[208:211], v[0:3]
	v_mfma_f32_16x16x32_bf16 v[52:55], v[172:175], v[188:191], v[52:55]
	v_mfma_f32_16x16x32_bf16 v[44:47], v[180:183], v[188:191], v[44:47]
	v_mfma_f32_16x16x32_bf16 v[36:39], v[172:175], v[196:199], v[36:39]
	v_mfma_f32_16x16x32_bf16 v[28:31], v[180:183], v[196:199], v[28:31]
	v_mfma_f32_16x16x32_bf16 v[20:23], v[172:175], v[204:207], v[20:23]
	v_mfma_f32_16x16x32_bf16 v[12:15], v[180:183], v[204:207], v[12:15]
	v_mfma_f32_16x16x32_bf16 v[4:7], v[172:175], v[212:215], v[4:7]
	v_mfma_f32_16x16x32_bf16 v[0:3], v[180:183], v[212:215], v[0:3]
	s_add_i32 s61, s61, 2
	s_add_u32 s36, s36, 0x100
	s_addc_u32 s37, s37, 0
	s_add_u32 s59, s59, 0x100
	s_addc_u32 s60, s60, 0
	s_cmp_gt_u32 s61, 13
	s_setprio 0
	s_barrier
	s_cbranch_scc0 .LBB0_1120
	s_and_b64 vcc, exec, s[12:13]
	s_cbranch_vccz .LBB0_1123
	s_barrier

; #define PG8_STAGE(bufoff, gbase, voff) do { _Pragma("unroll") for (int _i = 0; _i < 2; ++_i) \
;         __builtin_amdgcn_global_load_lds((const unsigned*)((const char*)(gbase) + (voff)[_i]), (PG8_LAS unsigned*)(lds + (bufoff) + ldsw + _i * 8192), 16, 0, 0); } while (0)
; #define PG8_WAIT_V(n) asm volatile("s_waitcnt vmcnt(" #n ")" ::: "memory")
; #define PG8_WAIT_L(n) asm volatile("s_waitcnt lgkmcnt(" #n ")" ::: "memory")
; #define PG8_BAR __builtin_amdgcn_s_barrier()
; #define PG8_SCHED __builtin_amdgcn_sched_barrier(0)
; template <class Epi, class Sched, bool ALIGN_EPI = false, bool SP2 = false, bool FP8 = false, bool PEEL = false>
; __device__ __forceinline__ void gemm_phase(PG8_LAS unsigned char* lds, const Gemm g, const Sched& S, const Epi& E, const int wid) {
;     ...
;             const bool last = (t == nt - 2);
;             const char* a1 = cA + (size_t)(t + 1) * kstep;
;             const char* a2 = last ? nA : cA + (size_t)(t + 2) * kstep; const char* b2 = last ? nB : cB + (size_t)(t + 2) * kstep;
;             const char* a3 = a2 + kstep; const char* b3 = b2 + kstep;
;             if (last && has_next) S.a_ready(nxt);
;             PG8_LDB(B0, 0, 0); PG8_LDB(B1, 0, 1); PG8_SCHED; PG8_LDA(At, 0, 0); PG8_STAGE(PG8_SA(1, 1), a1 + hstep, voffA);
;             PG8_WAIT_V(8); PG8_WAIT_L(0); PG8_BAR; PG8_MMA(0, 0, At, B0); PG8_MMA(0, 1, At, B1); PG8_BAR; PG8_SCHED;
.LBB0_1535:
	ds_read_b128 v[128:131], v209
	ds_read_b128 v[132:135], v209 offset:1024
	ds_read_b128 v[136:139], v209 offset:2048
	ds_read_b128 v[140:143], v209 offset:3072
	ds_read_b128 v[144:147], v210
	ds_read_b128 v[148:151], v210 offset:1024
	ds_read_b128 v[152:155], v210 offset:2048
	ds_read_b128 v[156:159], v210 offset:3072
	s_add_u32 s30, s26, 0xfffc0080
	s_addc_u32 s31, s27, -1
	s_cmp_eq_u32 s67, 12
	s_cselect_b32 s37, s15, s31
	s_cselect_b32 s36, s63, s30
	s_cselect_b32 s31, s13, s66
	s_cselect_b32 s30, s64, s65
	v_lshl_add_u64 v[204:205], s[26:27], 0, v[196:197]
	s_add_i32 m0, s41, 0xc000
	ds_read_b128 v[160:163], v211
	ds_read_b128 v[164:167], v211 offset:1024
	ds_read_b128 v[168:171], v211 offset:2048
	ds_read_b128 v[172:175], v211 offset:3072
	ds_read_b128 v[176:179], v211 offset:4096
	ds_read_b128 v[180:183], v211 offset:5120
	ds_read_b128 v[184:187], v211 offset:6144
	ds_read_b128 v[212:215], v211 offset:7168
	global_load_lds_dwordx4 v[204:205], off
	v_lshl_add_u64 v[204:205], s[26:27], 0, v[198:199]
	s_add_i32 m0, s41, 0xe000
	s_nop 0
	global_load_lds_dwordx4 v[204:205], off
	s_waitcnt vmcnt(8)
	s_waitcnt lgkmcnt(0)
	s_barrier
	s_setprio 1
	s_waitcnt lgkmcnt(0)
	v_mfma_f32_16x16x32_bf16 v[124:127], v[128:131], v[160:163], v[124:127]
	v_mfma_f32_16x16x32_bf16 v[120:123], v[136:139], v[160:163], v[120:123]
	v_mfma_f32_16x16x32_bf16 v[108:111], v[128:131], v[168:171], v[108:111]
	v_mfma_f32_16x16x32_bf16 v[104:107], v[136:139], v[168:171], v[104:107]
	v_mfma_f32_16x16x32_bf16 v[92:95], v[128:131], v[176:179], v[92:95]
	v_mfma_f32_16x16x32_bf16 v[88:91], v[136:139], v[176:179], v[88:91]
	v_mfma_f32_16x16x32_bf16 v[76:79], v[128:131], v[184:187], v[76:79]
	v_mfma_f32_16x16x32_bf16 v[72:75], v[136:139], v[184:187], v[72:75]
	v_mfma_f32_16x16x32_bf16 v[124:127], v[132:135], v[164:167], v[124:127]
	v_mfma_f32_16x16x32_bf16 v[120:123], v[140:143], v[164:167], v[120:123]
	v_mfma_f32_16x16x32_bf16 v[108:111], v[132:135], v[172:175], v[108:111]
	v_mfma_f32_16x16x32_bf16 v[104:107], v[140:143], v[172:175], v[104:107]
	v_mfma_f32_16x16x32_bf16 v[92:95], v[132:135], v[180:183], v[92:95]
	v_mfma_f32_16x16x32_bf16 v[88:91], v[140:143], v[180:183], v[88:91]
	v_mfma_f32_16x16x32_bf16 v[76:79], v[132:135], v[212:215], v[76:79]
	v_mfma_f32_16x16x32_bf16 v[72:75], v[140:143], v[212:215], v[72:75]
	s_setprio 0
	s_setprio 1
	v_mfma_f32_16x16x32_bf16 v[116:119], v[144:147], v[160:163], v[116:119]
	v_mfma_f32_16x16x32_bf16 v[112:115], v[152:155], v[160:163], v[112:115]
	v_mfma_f32_16x16x32_bf16 v[100:103], v[144:147], v[168:171], v[100:103]
	v_mfma_f32_16x16x32_bf16 v[96:99], v[152:155], v[168:171], v[96:99]
	v_mfma_f32_16x16x32_bf16 v[84:87], v[144:147], v[176:179], v[84:87]
	v_mfma_f32_16x16x32_bf16 v[80:83], v[152:155], v[176:179], v[80:83]
	v_mfma_f32_16x16x32_bf16 v[68:71], v[144:147], v[184:187], v[68:71]
	v_mfma_f32_16x16x32_bf16 v[64:67], v[152:155], v[184:187], v[64:67]
	v_mfma_f32_16x16x32_bf16 v[116:119], v[148:151], v[164:167], v[116:119]
	v_mfma_f32_16x16x32_bf16 v[112:115], v[156:159], v[164:167], v[112:115]
	v_mfma_f32_16x16x32_bf16 v[100:103], v[148:151], v[172:175], v[100:103]
	v_mfma_f32_16x16x32_bf16 v[96:99], v[156:159], v[172:175], v[96:99]
	v_mfma_f32_16x16x32_bf16 v[84:87], v[148:151], v[180:183], v[84:87]
	v_mfma_f32_16x16x32_bf16 v[80:83], v[156:159], v[180:183], v[80:83]
	v_mfma_f32_16x16x32_bf16 v[68:71], v[148:151], v[212:215], v[68:71]
	v_mfma_f32_16x16x32_bf16 v[64:67], v[156:159], v[212:215], v[64:67]
	s_setprio 0
	s_barrier
	s_add_i32 s75, s54, s39
	v_lshl_add_u64 v[204:205], s[30:31], 0, v[192:193]
	s_mov_b32 m0, s75
	ds_read_b128 v[160:163], v211 offset:16384
	ds_read_b128 v[164:167], v211 offset:17408
	ds_read_b128 v[168:171], v211 offset:18432
	ds_read_b128 v[172:175], v211 offset:19456
	ds_read_b128 v[176:179], v211 offset:20480
	ds_read_b128 v[180:183], v211 offset:21504
	ds_read_b128 v[184:187], v211 offset:22528
	ds_read_b128 v[212:215], v211 offset:23552
	global_load_lds_dwordx4 v[204:205], off
	s_add_i32 m0, s75, 0x2000
	s_add_u32 s80, s30, 0x40000
	v_lshl_add_u64 v[216:217], s[30:31], 0, v[188:189]
	s_addc_u32 s81, s31, 0
	s_add_i32 s75, s55, s39
	global_load_lds_dwordx4 v[216:217], off
	v_lshl_add_u64 v[218:219], s[80:81], 0, v[192:193]
	s_mov_b32 m0, s75
	v_lshl_add_u64 v[220:221], s[36:37], 0, v[190:191]
	global_load_lds_dwordx4 v[218:219], off
	v_lshl_add_u64 v[218:219], s[80:81], 0, v[188:189]
	s_add_i32 m0, s75, 0x2000
	s_nop 0
	global_load_lds_dwordx4 v[218:219], off
	v_lshl_add_u64 v[218:219], s[36:37], 0, v[194:195]
	s_mov_b32 m0, s41
	s_nop 0
	global_load_lds_dwordx4 v[218:219], off
	s_mov_b32 m0, s42
	s_nop 0
	global_load_lds_dwordx4 v[220:221], off
	s_waitcnt vmcnt(8)
	s_waitcnt lgkmcnt(0)
	s_barrier
; #define PG8_STAGE(bufoff, gbase, voff) do { _Pragma("unroll") for (int _i = 0; _i < 2; ++_i) \
;         __builtin_amdgcn_global_load_lds((const unsigned*)((const char*)(gbase) + (voff)[_i]), (PG8_LAS unsigned*)(lds + (bufoff) + ldsw + _i * 8192), 16, 0, 0); } while (0)
; #define PG8_WAIT_V(n) asm volatile("s_waitcnt vmcnt(" #n ")" ::: "memory")
; #define PG8_WAIT_L(n) asm volatile("s_waitcnt lgkmcnt(" #n ")" ::: "memory")
; #define PG8_BAR __builtin_amdgcn_s_barrier()
; #define PG8_SCHED __builtin_amdgcn_sched_barrier(0)
; template <class Epi, class Sched, bool ALIGN_EPI = false, bool SP2 = false, bool FP8 = false, bool PEEL = false>
; __device__ __forceinline__ void gemm_phase(PG8_LAS unsigned char* lds, const Gemm g, const Sched& S, const Epi& E, const int wid) {
;     ...
;             PG8_WAIT_V(8); PG8_WAIT_L(0); PG8_BAR; PG8_MMA(1, 0, At, B0); PG8_MMA(1, 1, At, B1); PG8_BAR; PG8_SCHED;
;             PG8_LDB(B0, 1, 0); PG8_LDB(B1, 1, 1); PG8_SCHED; PG8_LDA(At, 1, 0); PG8_STAGE(PG8_SA(0, 1), a2 + hstep, voffA);
;             PG8_WAIT_V(8); PG8_WAIT_L(0); PG8_BAR; PG8_MMA(0, 0, At, B0); PG8_MMA(0, 1, At, B1); PG8_BAR; PG8_SCHED;
	s_setprio 1
	s_waitcnt lgkmcnt(0)
	v_mfma_f32_16x16x32_bf16 v[60:63], v[128:131], v[160:163], v[60:63]
	v_mfma_f32_16x16x32_bf16 v[56:59], v[136:139], v[160:163], v[56:59]
	v_mfma_f32_16x16x32_bf16 v[44:47], v[128:131], v[168:171], v[44:47]
	v_mfma_f32_16x16x32_bf16 v[40:43], v[136:139], v[168:171], v[40:43]
	v_mfma_f32_16x16x32_bf16 v[28:31], v[128:131], v[176:179], v[28:31]
	v_mfma_f32_16x16x32_bf16 v[24:27], v[136:139], v[176:179], v[24:27]
	v_mfma_f32_16x16x32_bf16 v[12:15], v[128:131], v[184:187], v[12:15]
	v_mfma_f32_16x16x32_bf16 v[8:11], v[136:139], v[184:187], v[8:11]
	v_mfma_f32_16x16x32_bf16 v[60:63], v[132:135], v[164:167], v[60:63]
	v_mfma_f32_16x16x32_bf16 v[56:59], v[140:143], v[164:167], v[56:59]
	v_mfma_f32_16x16x32_bf16 v[44:47], v[132:135], v[172:175], v[44:47]
	v_mfma_f32_16x16x32_bf16 v[40:43], v[140:143], v[172:175], v[40:43]
	v_mfma_f32_16x16x32_bf16 v[28:31], v[132:135], v[180:183], v[28:31]
	v_mfma_f32_16x16x32_bf16 v[24:27], v[140:143], v[180:183], v[24:27]
	v_mfma_f32_16x16x32_bf16 v[12:15], v[132:135], v[212:215], v[12:15]
	v_mfma_f32_16x16x32_bf16 v[8:11], v[140:143], v[212:215], v[8:11]
	s_setprio 0
	s_setprio 1
	v_mfma_f32_16x16x32_bf16 v[52:55], v[144:147], v[160:163], v[52:55]
	v_mfma_f32_16x16x32_bf16 v[48:51], v[152:155], v[160:163], v[48:51]
	v_mfma_f32_16x16x32_bf16 v[36:39], v[144:147], v[168:171], v[36:39]
	v_mfma_f32_16x16x32_bf16 v[32:35], v[152:155], v[168:171], v[32:35]
	v_mfma_f32_16x16x32_bf16 v[20:23], v[144:147], v[176:179], v[20:23]
	v_mfma_f32_16x16x32_bf16 v[16:19], v[152:155], v[176:179], v[16:19]
	v_mfma_f32_16x16x32_bf16 v[4:7], v[144:147], v[184:187], v[4:7]
	v_mfma_f32_16x16x32_bf16 v[0:3], v[152:155], v[184:187], v[0:3]
	v_mfma_f32_16x16x32_bf16 v[52:55], v[148:151], v[164:167], v[52:55]
	v_mfma_f32_16x16x32_bf16 v[48:51], v[156:159], v[164:167], v[48:51]
	v_mfma_f32_16x16x32_bf16 v[36:39], v[148:151], v[172:175], v[36:39]
	v_mfma_f32_16x16x32_bf16 v[32:35], v[156:159], v[172:175], v[32:35]
	v_mfma_f32_16x16x32_bf16 v[20:23], v[148:151], v[180:183], v[20:23]
	v_mfma_f32_16x16x32_bf16 v[16:19], v[156:159], v[180:183], v[16:19]
	v_mfma_f32_16x16x32_bf16 v[4:7], v[148:151], v[212:215], v[4:7]
	v_mfma_f32_16x16x32_bf16 v[0:3], v[156:159], v[212:215], v[0:3]
	s_setprio 0
	s_barrier
	s_add_i32 s75, 0, 0x18000
	s_add_i32 s80, 0, 0x1c000
	v_add_u32_e32 v140, s75, v207
	v_add_u32_e32 v156, s80, v207
	ds_read_b128 v[128:131], v140
	ds_read_b128 v[132:135], v140 offset:1024
	ds_read_b128 v[136:139], v140 offset:2048
	ds_read_b128 v[140:143], v140 offset:3072
	ds_read_b128 v[144:147], v156
	ds_read_b128 v[148:151], v156 offset:1024
	ds_read_b128 v[152:155], v156 offset:2048
	ds_read_b128 v[156:159], v156 offset:3072
	s_add_u32 s36, s36, 0x40000
	s_addc_u32 s37, s37, 0
	s_mov_b32 m0, s43
	v_lshl_add_u64 v[222:223], s[36:37], 0, v[194:195]
	ds_read_b128 v[160:163], v211 offset:32768
	ds_read_b128 v[164:167], v211 offset:33792
	ds_read_b128 v[168:171], v211 offset:34816
	ds_read_b128 v[172:175], v211 offset:35840
	ds_read_b128 v[176:179], v211 offset:36864
	ds_read_b128 v[180:183], v211 offset:37888
	ds_read_b128 v[184:187], v211 offset:38912
	ds_read_b128 v[212:215], v211 offset:39936
	global_load_lds_dwordx4 v[222:223], off
	v_lshl_add_u64 v[222:223], s[36:37], 0, v[190:191]
	s_mov_b32 m0, s44
	s_nop 0
	global_load_lds_dwordx4 v[222:223], off
	s_waitcnt vmcnt(8)
	s_waitcnt lgkmcnt(0)
	s_barrier
	s_setprio 1
	s_waitcnt lgkmcnt(0)
	v_mfma_f32_16x16x32_bf16 v[124:127], v[128:131], v[160:163], v[124:127]
	v_mfma_f32_16x16x32_bf16 v[120:123], v[136:139], v[160:163], v[120:123]
	v_mfma_f32_16x16x32_bf16 v[108:111], v[128:131], v[168:171], v[108:111]
	v_mfma_f32_16x16x32_bf16 v[104:107], v[136:139], v[168:171], v[104:107]
	v_mfma_f32_16x16x32_bf16 v[92:95], v[128:131], v[176:179], v[92:95]
	v_mfma_f32_16x16x32_bf16 v[88:91], v[136:139], v[176:179], v[88:91]
	v_mfma_f32_16x16x32_bf16 v[76:79], v[128:131], v[184:187], v[76:79]
	v_mfma_f32_16x16x32_bf16 v[72:75], v[136:139], v[184:187], v[72:75]
	v_mfma_f32_16x16x32_bf16 v[124:127], v[132:135], v[164:167], v[124:127]
	v_mfma_f32_16x16x32_bf16 v[120:123], v[140:143], v[164:167], v[120:123]
	v_mfma_f32_16x16x32_bf16 v[108:111], v[132:135], v[172:175], v[108:111]
	v_mfma_f32_16x16x32_bf16 v[104:107], v[140:143], v[172:175], v[104:107]
	v_mfma_f32_16x16x32_bf16 v[92:95], v[132:135], v[180:183], v[92:95]
	v_mfma_f32_16x16x32_bf16 v[88:91], v[140:143], v[180:183], v[88:91]
	v_mfma_f32_16x16x32_bf16 v[76:79], v[132:135], v[212:215], v[76:79]
	v_mfma_f32_16x16x32_bf16 v[72:75], v[140:143], v[212:215], v[72:75]
	s_setprio 0
	s_setprio 1
	v_mfma_f32_16x16x32_bf16 v[116:119], v[144:147], v[160:163], v[116:119]
	v_mfma_f32_16x16x32_bf16 v[112:115], v[152:155], v[160:163], v[112:115]
	v_mfma_f32_16x16x32_bf16 v[100:103], v[144:147], v[168:171], v[100:103]
	v_mfma_f32_16x16x32_bf16 v[96:99], v[152:155], v[168:171], v[96:99]
	v_mfma_f32_16x16x32_bf16 v[84:87], v[144:147], v[176:179], v[84:87]
	v_mfma_f32_16x16x32_bf16 v[80:83], v[152:155], v[176:179], v[80:83]
	v_mfma_f32_16x16x32_bf16 v[68:71], v[144:147], v[184:187], v[68:71]
	v_mfma_f32_16x16x32_bf16 v[64:67], v[152:155], v[184:187], v[64:67]
	v_mfma_f32_16x16x32_bf16 v[116:119], v[148:151], v[164:167], v[116:119]
	v_mfma_f32_16x16x32_bf16 v[112:115], v[156:159], v[164:167], v[112:115]
	v_mfma_f32_16x16x32_bf16 v[100:103], v[148:151], v[172:175], v[100:103]
	v_mfma_f32_16x16x32_bf16 v[96:99], v[156:159], v[172:175], v[96:99]
	v_mfma_f32_16x16x32_bf16 v[84:87], v[148:151], v[180:183], v[84:87]
	v_mfma_f32_16x16x32_bf16 v[80:83], v[156:159], v[180:183], v[80:83]
	v_mfma_f32_16x16x32_bf16 v[68:71], v[148:151], v[212:215], v[68:71]
	v_mfma_f32_16x16x32_bf16 v[64:67], v[156:159], v[212:215], v[64:67]
	s_setprio 0
	s_barrier
; #define PG8_STAGE(bufoff, gbase, voff) do { _Pragma("unroll") for (int _i = 0; _i < 2; ++_i) \
;         __builtin_amdgcn_global_load_lds((const unsigned*)((const char*)(gbase) + (voff)[_i]), (PG8_LAS unsigned*)(lds + (bufoff) + ldsw + _i * 8192), 16, 0, 0); } while (0)
; #define PG8_WAIT_V(n) asm volatile("s_waitcnt vmcnt(" #n ")" ::: "memory")
; #define PG8_WAIT_L(n) asm volatile("s_waitcnt lgkmcnt(" #n ")" ::: "memory")
; #define PG8_BAR __builtin_amdgcn_s_barrier()
; #define PG8_SCHED __builtin_amdgcn_sched_barrier(0)
; template <class Epi, class Sched, bool ALIGN_EPI = false, bool SP2 = false, bool FP8 = false, bool PEEL = false>
; __device__ __forceinline__ void gemm_phase(PG8_LAS unsigned char* lds, const Gemm g, const Sched& S, const Epi& E, const int wid) {
;     ...
;         for (int t = 2; t < nt; t += 2) {
;     ...
;             PG8_LDA(At, 1, 1); PG8_STAGE(PG8_SB(1, 0), b3, voffB); PG8_STAGE(PG8_SB(1, 1), b3 + hstep, voffB); PG8_STAGE(PG8_SA(1, 0), a3, voffA);
;             PG8_WAIT_V(8); PG8_WAIT_L(0); PG8_BAR; PG8_MMA(1, 0, At, B0); PG8_MMA(1, 1, At, B1); PG8_BAR; PG8_SCHED;
	s_add_i32 s36, s75, s39
	v_lshl_add_u64 v[204:205], v[204:205], 0, s[10:11]
	s_mov_b32 m0, s36
	ds_read_b128 v[160:163], v211 offset:49152
	ds_read_b128 v[164:167], v211 offset:50176
	ds_read_b128 v[168:171], v211 offset:51200
	ds_read_b128 v[172:175], v211 offset:52224
	ds_read_b128 v[176:179], v211 offset:53248
	ds_read_b128 v[180:183], v211 offset:54272
	ds_read_b128 v[184:187], v211 offset:55296
	ds_read_b128 v[212:215], v211 offset:56320
	global_load_lds_dwordx4 v[204:205], off
	s_add_i32 m0, s36, 0x2000
	s_add_u32 s30, s30, 0x40080
	v_lshl_add_u64 v[204:205], v[216:217], 0, s[10:11]
	s_addc_u32 s31, s31, 0
	s_add_i32 s36, s80, s39
	global_load_lds_dwordx4 v[204:205], off
	v_lshl_add_u64 v[204:205], s[30:31], 0, v[192:193]
	s_mov_b32 m0, s36
	s_nop 0
	global_load_lds_dwordx4 v[204:205], off
	v_lshl_add_u64 v[204:205], s[30:31], 0, v[188:189]
	s_add_i32 m0, s36, 0x2000
	s_nop 0
	global_load_lds_dwordx4 v[204:205], off
	v_lshl_add_u64 v[204:205], v[218:219], 0, s[10:11]
	s_mov_b32 m0, s50
	s_nop 0
	global_load_lds_dwordx4 v[204:205], off
	v_lshl_add_u64 v[204:205], v[220:221], 0, s[10:11]
	s_mov_b32 m0, s51
	s_nop 0
	global_load_lds_dwordx4 v[204:205], off
	s_waitcnt vmcnt(8)
	s_waitcnt lgkmcnt(0)
	s_barrier
	s_setprio 1
	s_waitcnt lgkmcnt(0)
	v_mfma_f32_16x16x32_bf16 v[60:63], v[128:131], v[160:163], v[60:63]
	v_mfma_f32_16x16x32_bf16 v[56:59], v[136:139], v[160:163], v[56:59]
	v_mfma_f32_16x16x32_bf16 v[44:47], v[128:131], v[168:171], v[44:47]
	v_mfma_f32_16x16x32_bf16 v[40:43], v[136:139], v[168:171], v[40:43]
	v_mfma_f32_16x16x32_bf16 v[28:31], v[128:131], v[176:179], v[28:31]
	v_mfma_f32_16x16x32_bf16 v[24:27], v[136:139], v[176:179], v[24:27]
	v_mfma_f32_16x16x32_bf16 v[12:15], v[128:131], v[184:187], v[12:15]
	v_mfma_f32_16x16x32_bf16 v[8:11], v[136:139], v[184:187], v[8:11]
	v_mfma_f32_16x16x32_bf16 v[60:63], v[132:135], v[164:167], v[60:63]
	v_mfma_f32_16x16x32_bf16 v[56:59], v[140:143], v[164:167], v[56:59]
	v_mfma_f32_16x16x32_bf16 v[44:47], v[132:135], v[172:175], v[44:47]
	v_mfma_f32_16x16x32_bf16 v[40:43], v[140:143], v[172:175], v[40:43]
	v_mfma_f32_16x16x32_bf16 v[28:31], v[132:135], v[180:183], v[28:31]
	v_mfma_f32_16x16x32_bf16 v[24:27], v[140:143], v[180:183], v[24:27]
	v_mfma_f32_16x16x32_bf16 v[12:15], v[132:135], v[212:215], v[12:15]
	v_mfma_f32_16x16x32_bf16 v[8:11], v[140:143], v[212:215], v[8:11]
	s_setprio 0
	s_setprio 1
	v_mfma_f32_16x16x32_bf16 v[52:55], v[144:147], v[160:163], v[52:55]
	v_mfma_f32_16x16x32_bf16 v[48:51], v[152:155], v[160:163], v[48:51]
	v_mfma_f32_16x16x32_bf16 v[36:39], v[144:147], v[168:171], v[36:39]
	v_mfma_f32_16x16x32_bf16 v[32:35], v[152:155], v[168:171], v[32:35]
	v_mfma_f32_16x16x32_bf16 v[20:23], v[144:147], v[176:179], v[20:23]
	v_mfma_f32_16x16x32_bf16 v[16:19], v[152:155], v[176:179], v[16:19]
	v_mfma_f32_16x16x32_bf16 v[4:7], v[144:147], v[184:187], v[4:7]
	v_mfma_f32_16x16x32_bf16 v[0:3], v[152:155], v[184:187], v[0:3]
	v_mfma_f32_16x16x32_bf16 v[52:55], v[148:151], v[164:167], v[52:55]
	v_mfma_f32_16x16x32_bf16 v[48:51], v[156:159], v[164:167], v[48:51]
	v_mfma_f32_16x16x32_bf16 v[36:39], v[148:151], v[172:175], v[36:39]
	v_mfma_f32_16x16x32_bf16 v[32:35], v[156:159], v[172:175], v[32:35]
	v_mfma_f32_16x16x32_bf16 v[20:23], v[148:151], v[180:183], v[20:23]
	v_mfma_f32_16x16x32_bf16 v[16:19], v[156:159], v[180:183], v[16:19]
	v_mfma_f32_16x16x32_bf16 v[4:7], v[148:151], v[212:215], v[4:7]
	v_mfma_f32_16x16x32_bf16 v[0:3], v[156:159], v[212:215], v[0:3]
	s_add_i32 s67, s67, 2
	s_add_u32 s26, s26, 0x100
	s_addc_u32 s27, s27, 0
	s_add_u32 s65, s65, 0x100
	s_addc_u32 s66, s66, 0
	s_cmp_gt_u32 s67, 13
	s_setprio 0
	s_barrier
	s_cbranch_scc0 .LBB0_1535
	s_and_b64 vcc, exec, s[8:9]
	s_cbranch_vccz .LBB0_1538
	s_barrier

; #define PG8_STAGE(bufoff, gbase, voff) do { _Pragma("unroll") for (int _i = 0; _i < 2; ++_i) \
;         __builtin_amdgcn_global_load_lds((const unsigned*)((const char*)(gbase) + (voff)[_i]), (PG8_LAS unsigned*)(lds + (bufoff) + ldsw + _i * 8192), 16, 0, 0); } while (0)
; #define PG8_WAIT_V(n) asm volatile("s_waitcnt vmcnt(" #n ")" ::: "memory")
; #define PG8_WAIT_L(n) asm volatile("s_waitcnt lgkmcnt(" #n ")" ::: "memory")
; #define PG8_BAR __builtin_amdgcn_s_barrier()
; #define PG8_SCHED __builtin_amdgcn_sched_barrier(0)
; template <class Epi, class Sched, bool ALIGN_EPI = false, bool SP2 = false, bool FP8 = false, bool PEEL = false>
; __device__ __forceinline__ void gemm_phase(PG8_LAS unsigned char* lds, const Gemm g, const Sched& S, const Epi& E, const int wid) {
;     ...
;             const bool last = (t == nt - 2);
;             const char* a1 = cA + (size_t)(t + 1) * kstep;
;             const char* a2 = last ? nA : cA + (size_t)(t + 2) * kstep; const char* b2 = last ? nB : cB + (size_t)(t + 2) * kstep;
;             const char* a3 = a2 + kstep; const char* b3 = b2 + kstep;
;             if (last && has_next) S.a_ready(nxt);
;             PG8_LDB(B0, 0, 0); PG8_LDB(B1, 0, 1); PG8_SCHED; PG8_LDA(At, 0, 0); PG8_STAGE(PG8_SA(1, 1), a1 + hstep, voffA);
;             PG8_WAIT_V(8); PG8_WAIT_L(0); PG8_BAR; PG8_MMA(0, 0, At, B0); PG8_MMA(0, 1, At, B1); PG8_BAR; PG8_SCHED;
.LBB0_1761:
	ds_read_b128 v[0:3], v186
	ds_read_b128 v[4:7], v186 offset:1024
	ds_read_b128 v[16:19], v186 offset:2048
	ds_read_b128 v[20:23], v186 offset:3072
	ds_read_b128 v[24:27], v187
	ds_read_b128 v[28:31], v187 offset:1024
	ds_read_b128 v[174:177], v187 offset:2048
	ds_read_b128 v[178:181], v187 offset:3072
	s_add_u32 s38, s40, 0xfffe0080
	s_addc_u32 s39, s41, -1
	s_cmp_eq_u32 s89, 4
	s_cselect_b32 s43, s25, s39
	s_cselect_b32 s42, s27, s38
	s_cselect_b32 s39, s75, s88
	s_cselect_b32 s38, s76, s87
	s_mov_b32 m0, s77
	v_lshl_add_u64 v[214:215], s[40:41], 0, v[168:169]
	ds_read_b128 v[8:11], v185
	ds_read_b128 v[12:15], v185 offset:1024
	ds_read_b128 v[190:193], v185 offset:2048
	ds_read_b128 v[194:197], v185 offset:3072
	ds_read_b128 v[198:201], v185 offset:4096
	ds_read_b128 v[202:205], v185 offset:5120
	ds_read_b128 v[206:209], v185 offset:6144
	ds_read_b128 v[210:213], v185 offset:7168
	global_load_lds_dwordx4 v[214:215], off
	v_lshl_add_u64 v[214:215], s[40:41], 0, v[170:171]
	s_mov_b32 m0, s78
	s_nop 0
	global_load_lds_dwordx4 v[214:215], off
	s_waitcnt vmcnt(8)
	s_waitcnt lgkmcnt(0)
	s_barrier
	s_setprio 1
	s_waitcnt lgkmcnt(0)
	v_mfma_f32_16x16x128_f8f6f4 v[156:159], v[0:7], v[8:15], v[156:159]
	v_mfma_f32_16x16x128_f8f6f4 v[152:155], v[16:23], v[8:15], v[152:155]
	v_mfma_f32_16x16x128_f8f6f4 v[148:151], v[0:7], v[190:197], v[148:151]
	v_mfma_f32_16x16x128_f8f6f4 v[144:147], v[16:23], v[190:197], v[144:147]
	v_mfma_f32_16x16x128_f8f6f4 v[140:143], v[0:7], v[198:205], v[140:143]
	v_mfma_f32_16x16x128_f8f6f4 v[136:139], v[16:23], v[198:205], v[136:139]
	v_mfma_f32_16x16x128_f8f6f4 v[132:135], v[0:7], v[206:213], v[132:135]
	v_mfma_f32_16x16x128_f8f6f4 v[128:131], v[16:23], v[206:213], v[128:131]
	s_setprio 0
	s_setprio 1
	v_mfma_f32_16x16x128_f8f6f4 v[124:127], v[24:31], v[8:15], v[124:127]
	v_mfma_f32_16x16x128_f8f6f4 v[120:123], v[174:181], v[8:15], v[120:123]
	v_mfma_f32_16x16x128_f8f6f4 v[116:119], v[24:31], v[190:197], v[116:119]
	v_mfma_f32_16x16x128_f8f6f4 v[112:115], v[174:181], v[190:197], v[112:115]
	v_mfma_f32_16x16x128_f8f6f4 v[108:111], v[24:31], v[198:205], v[108:111]
	v_mfma_f32_16x16x128_f8f6f4 v[104:107], v[174:181], v[198:205], v[104:107]
	v_mfma_f32_16x16x128_f8f6f4 v[100:103], v[24:31], v[206:213], v[100:103]
	v_mfma_f32_16x16x128_f8f6f4 v[96:99], v[174:181], v[206:213], v[96:99]
	s_setprio 0
	s_barrier
	s_mov_b32 m0, s79
	v_lshl_add_u64 v[8:9], s[38:39], 0, v[162:163]
	s_add_u32 s90, s38, 0x20000
	ds_read_b128 v[190:193], v185 offset:16384
	ds_read_b128 v[194:197], v185 offset:17408
	ds_read_b128 v[198:201], v185 offset:18432
	ds_read_b128 v[202:205], v185 offset:19456
	ds_read_b128 v[206:209], v185 offset:20480
	ds_read_b128 v[210:213], v185 offset:21504
	ds_read_b128 v[214:217], v185 offset:22528
	ds_read_b128 v[218:221], v185 offset:23552
	global_load_lds_dwordx4 v[8:9], off
	v_lshl_add_u64 v[10:11], s[38:39], 0, v[166:167]
	s_mov_b32 m0, s80
	s_addc_u32 s91, s39, 0
	global_load_lds_dwordx4 v[10:11], off
	v_lshl_add_u64 v[12:13], s[90:91], 0, v[162:163]
	s_mov_b32 m0, s81
	v_lshl_add_u64 v[14:15], s[42:43], 0, v[164:165]
	global_load_lds_dwordx4 v[12:13], off
	v_lshl_add_u64 v[12:13], s[90:91], 0, v[166:167]
	s_mov_b32 m0, s82
	s_nop 0
	global_load_lds_dwordx4 v[12:13], off
	v_lshl_add_u64 v[12:13], s[42:43], 0, v[160:161]
	s_mov_b32 m0, s54
	s_nop 0
	global_load_lds_dwordx4 v[12:13], off
	s_mov_b32 m0, s55
	s_nop 0
	global_load_lds_dwordx4 v[14:15], off
	s_waitcnt vmcnt(8)
	s_waitcnt lgkmcnt(0)
	s_barrier
	s_setprio 1
	s_waitcnt lgkmcnt(0)
	v_mfma_f32_16x16x128_f8f6f4 v[92:95], v[0:7], v[190:197], v[92:95]
	v_mfma_f32_16x16x128_f8f6f4 v[88:91], v[16:23], v[190:197], v[88:91]
	v_mfma_f32_16x16x128_f8f6f4 v[84:87], v[0:7], v[198:205], v[84:87]
	v_mfma_f32_16x16x128_f8f6f4 v[80:83], v[16:23], v[198:205], v[80:83]
	v_mfma_f32_16x16x128_f8f6f4 v[76:79], v[0:7], v[206:213], v[76:79]
	v_mfma_f32_16x16x128_f8f6f4 v[72:75], v[16:23], v[206:213], v[72:75]
	v_mfma_f32_16x16x128_f8f6f4 v[68:71], v[0:7], v[214:221], v[68:71]
	v_mfma_f32_16x16x128_f8f6f4 v[64:67], v[16:23], v[214:221], v[64:67]
	s_setprio 0
	s_setprio 1
	v_mfma_f32_16x16x128_f8f6f4 v[60:63], v[24:31], v[190:197], v[60:63]
	v_mfma_f32_16x16x128_f8f6f4 v[56:59], v[174:181], v[190:197], v[56:59]
	v_mfma_f32_16x16x128_f8f6f4 v[52:55], v[24:31], v[198:205], v[52:55]
	v_mfma_f32_16x16x128_f8f6f4 v[48:51], v[174:181], v[198:205], v[48:51]
	v_mfma_f32_16x16x128_f8f6f4 v[44:47], v[24:31], v[206:213], v[44:47]
	v_mfma_f32_16x16x128_f8f6f4 v[40:43], v[174:181], v[206:213], v[40:43]
	v_mfma_f32_16x16x128_f8f6f4 v[36:39], v[24:31], v[214:221], v[36:39]
	v_mfma_f32_16x16x128_f8f6f4 v[32:35], v[174:181], v[214:221], v[32:35]
	s_setprio 0
	s_barrier
; #define PG8_STAGE(bufoff, gbase, voff) do { _Pragma("unroll") for (int _i = 0; _i < 2; ++_i) \
;         __builtin_amdgcn_global_load_lds((const unsigned*)((const char*)(gbase) + (voff)[_i]), (PG8_LAS unsigned*)(lds + (bufoff) + ldsw + _i * 8192), 16, 0, 0); } while (0)
; #define PG8_WAIT_V(n) asm volatile("s_waitcnt vmcnt(" #n ")" ::: "memory")
; #define PG8_WAIT_L(n) asm volatile("s_waitcnt lgkmcnt(" #n ")" ::: "memory")
; #define PG8_BAR __builtin_amdgcn_s_barrier()
; #define PG8_SCHED __builtin_amdgcn_sched_barrier(0)
; template <class Epi, class Sched, bool ALIGN_EPI = false, bool SP2 = false, bool FP8 = false, bool PEEL = false>
; __device__ __forceinline__ void gemm_phase(PG8_LAS unsigned char* lds, const Gemm g, const Sched& S, const Epi& E, const int wid) {
;     ...
;         for (int t = 2; t < nt; t += 2) {
;     ...
;             PG8_LDA(At, 0, 1); PG8_STAGE(PG8_SB(0, 0), b2, voffB); PG8_STAGE(PG8_SB(0, 1), b2 + hstep, voffB); PG8_STAGE(PG8_SA(0, 0), a2, voffA);
;             PG8_WAIT_V(8); PG8_WAIT_L(0); PG8_BAR; PG8_MMA(1, 0, At, B0); PG8_MMA(1, 1, At, B1); PG8_BAR; PG8_SCHED;
;             PG8_LDB(B0, 1, 0); PG8_LDB(B1, 1, 1); PG8_SCHED; PG8_LDA(At, 1, 0); PG8_STAGE(PG8_SA(0, 1), a2 + hstep, voffA);
;             PG8_WAIT_V(8); PG8_WAIT_L(0); PG8_BAR; PG8_MMA(0, 0, At, B0); PG8_MMA(0, 1, At, B1); PG8_BAR; PG8_SCHED;
;             PG8_LDA(At, 1, 1); PG8_STAGE(PG8_SB(1, 0), b3, voffB); PG8_STAGE(PG8_SB(1, 1), b3 + hstep, voffB); PG8_STAGE(PG8_SA(1, 0), a3, voffA);
;             PG8_WAIT_V(8); PG8_WAIT_L(0); PG8_BAR; PG8_MMA(1, 0, At, B0); PG8_MMA(1, 1, At, B1); PG8_BAR; PG8_SCHED;
	ds_read_b128 v[16:19], v188
	ds_read_b128 v[20:23], v188 offset:1024
	ds_read_b128 v[24:27], v188 offset:2048
	ds_read_b128 v[28:31], v188 offset:3072
	ds_read_b128 v[0:3], v189
	ds_read_b128 v[4:7], v189 offset:1024
	ds_read_b128 v[174:177], v189 offset:2048
	ds_read_b128 v[178:181], v189 offset:3072
	s_add_u32 s42, s42, 0x20000
	s_addc_u32 s43, s43, 0
	s_mov_b32 m0, s56
	v_lshl_add_u64 v[222:223], s[42:43], 0, v[160:161]
	ds_read_b128 v[190:193], v185 offset:32768
	ds_read_b128 v[194:197], v185 offset:33792
	ds_read_b128 v[198:201], v185 offset:34816
	ds_read_b128 v[202:205], v185 offset:35840
	ds_read_b128 v[206:209], v185 offset:36864
	ds_read_b128 v[210:213], v185 offset:37888
	ds_read_b128 v[214:217], v185 offset:38912
	ds_read_b128 v[218:221], v185 offset:39936
	global_load_lds_dwordx4 v[222:223], off
	v_lshl_add_u64 v[222:223], s[42:43], 0, v[164:165]
	s_mov_b32 m0, s57
	s_nop 0
	global_load_lds_dwordx4 v[222:223], off
	s_waitcnt vmcnt(8)
	s_waitcnt lgkmcnt(0)
	s_barrier
	s_setprio 1
	s_waitcnt lgkmcnt(0)
	v_mfma_f32_16x16x128_f8f6f4 v[156:159], v[16:23], v[190:197], v[156:159]
	v_mfma_f32_16x16x128_f8f6f4 v[152:155], v[24:31], v[190:197], v[152:155]
	v_mfma_f32_16x16x128_f8f6f4 v[148:151], v[16:23], v[198:205], v[148:151]
	v_mfma_f32_16x16x128_f8f6f4 v[144:147], v[24:31], v[198:205], v[144:147]
	v_mfma_f32_16x16x128_f8f6f4 v[140:143], v[16:23], v[206:213], v[140:143]
	v_mfma_f32_16x16x128_f8f6f4 v[136:139], v[24:31], v[206:213], v[136:139]
	v_mfma_f32_16x16x128_f8f6f4 v[132:135], v[16:23], v[214:221], v[132:135]
	v_mfma_f32_16x16x128_f8f6f4 v[128:131], v[24:31], v[214:221], v[128:131]
	s_setprio 0
	s_setprio 1
	v_mfma_f32_16x16x128_f8f6f4 v[124:127], v[0:7], v[190:197], v[124:127]
	v_mfma_f32_16x16x128_f8f6f4 v[120:123], v[174:181], v[190:197], v[120:123]
	v_mfma_f32_16x16x128_f8f6f4 v[116:119], v[0:7], v[198:205], v[116:119]
	v_mfma_f32_16x16x128_f8f6f4 v[112:115], v[174:181], v[198:205], v[112:115]
	v_mfma_f32_16x16x128_f8f6f4 v[108:111], v[0:7], v[206:213], v[108:111]
	v_mfma_f32_16x16x128_f8f6f4 v[104:107], v[174:181], v[206:213], v[104:107]
	v_mfma_f32_16x16x128_f8f6f4 v[100:103], v[0:7], v[214:221], v[100:103]
	v_mfma_f32_16x16x128_f8f6f4 v[96:99], v[174:181], v[214:221], v[96:99]
	s_setprio 0
	s_barrier
	s_mov_b32 m0, s83
	v_lshl_add_u64 v[8:9], v[8:9], 0, s[10:11]
	s_add_u32 s38, s38, 0x20080
	ds_read_b128 v[190:193], v185 offset:49152
	ds_read_b128 v[194:197], v185 offset:50176
	ds_read_b128 v[198:201], v185 offset:51200
	ds_read_b128 v[202:205], v185 offset:52224
	ds_read_b128 v[206:209], v185 offset:53248
	ds_read_b128 v[210:213], v185 offset:54272
	ds_read_b128 v[214:217], v185 offset:55296
	ds_read_b128 v[218:221], v185 offset:56320
	global_load_lds_dwordx4 v[8:9], off
	v_lshl_add_u64 v[8:9], v[10:11], 0, s[10:11]
	s_mov_b32 m0, s84
	s_addc_u32 s39, s39, 0
	global_load_lds_dwordx4 v[8:9], off
	v_lshl_add_u64 v[8:9], s[38:39], 0, v[162:163]
	s_mov_b32 m0, s85
	s_nop 0
	global_load_lds_dwordx4 v[8:9], off
	v_lshl_add_u64 v[8:9], s[38:39], 0, v[166:167]
	s_mov_b32 m0, s86
	s_nop 0
	global_load_lds_dwordx4 v[8:9], off
	v_lshl_add_u64 v[8:9], v[12:13], 0, s[10:11]
	s_mov_b32 m0, s60
	s_nop 0
	global_load_lds_dwordx4 v[8:9], off
	v_lshl_add_u64 v[8:9], v[14:15], 0, s[10:11]
	s_mov_b32 m0, s61
	s_nop 0
	global_load_lds_dwordx4 v[8:9], off
	s_waitcnt vmcnt(8)
	s_waitcnt lgkmcnt(0)
	s_barrier
	s_setprio 1
	s_waitcnt lgkmcnt(0)
	v_mfma_f32_16x16x128_f8f6f4 v[92:95], v[16:23], v[190:197], v[92:95]
	v_mfma_f32_16x16x128_f8f6f4 v[88:91], v[24:31], v[190:197], v[88:91]
	v_mfma_f32_16x16x128_f8f6f4 v[84:87], v[16:23], v[198:205], v[84:87]
	v_mfma_f32_16x16x128_f8f6f4 v[80:83], v[24:31], v[198:205], v[80:83]
	v_mfma_f32_16x16x128_f8f6f4 v[76:79], v[16:23], v[206:213], v[76:79]
	v_mfma_f32_16x16x128_f8f6f4 v[72:75], v[24:31], v[206:213], v[72:75]
	v_mfma_f32_16x16x128_f8f6f4 v[68:71], v[16:23], v[214:221], v[68:71]
	v_mfma_f32_16x16x128_f8f6f4 v[64:67], v[24:31], v[214:221], v[64:67]
	s_setprio 0
	s_setprio 1
	v_mfma_f32_16x16x128_f8f6f4 v[60:63], v[0:7], v[190:197], v[60:63]
	v_mfma_f32_16x16x128_f8f6f4 v[56:59], v[174:181], v[190:197], v[56:59]
	v_mfma_f32_16x16x128_f8f6f4 v[52:55], v[0:7], v[198:205], v[52:55]
	v_mfma_f32_16x16x128_f8f6f4 v[48:51], v[174:181], v[198:205], v[48:51]
	v_mfma_f32_16x16x128_f8f6f4 v[44:47], v[0:7], v[206:213], v[44:47]
	v_mfma_f32_16x16x128_f8f6f4 v[40:43], v[174:181], v[206:213], v[40:43]
	v_mfma_f32_16x16x128_f8f6f4 v[36:39], v[0:7], v[214:221], v[36:39]
	v_mfma_f32_16x16x128_f8f6f4 v[32:35], v[174:181], v[214:221], v[32:35]
	s_add_i32 s89, s89, 2
	s_add_u32 s40, s40, 0x100
	s_addc_u32 s41, s41, 0
	s_add_u32 s87, s87, 0x100
	s_addc_u32 s88, s88, 0
	s_cmp_gt_u32 s89, 5
	s_setprio 0
	s_barrier
	s_cbranch_scc0 .LBB0_1761
	v_readlane_b32 s76, v254, 57
	s_and_b64 vcc, exec, s[8:9]
	v_readlane_b32 s77, v254, 58
	v_readlane_b32 s78, v254, 59
	v_readlane_b32 s79, v254, 60
	v_readlane_b32 s80, v254, 61
	v_readlane_b32 s81, v254, 62
	v_readlane_b32 s82, v254, 63
	v_readlane_b32 s83, v255, 0
	s_cbranch_vccz .LBB0_1764
	s_barrier

; #define PG8_STAGE(bufoff, gbase, voff) do { _Pragma("unroll") for (int _i = 0; _i < 2; ++_i) \
;         __builtin_amdgcn_global_load_lds((const unsigned*)((const char*)(gbase) + (voff)[_i]), (PG8_LAS unsigned*)(lds + (bufoff) + ldsw + _i * 8192), 16, 0, 0); } while (0)
; #define PG8_WAIT_V(n) asm volatile("s_waitcnt vmcnt(" #n ")" ::: "memory")
; #define PG8_WAIT_L(n) asm volatile("s_waitcnt lgkmcnt(" #n ")" ::: "memory")
; #define PG8_BAR __builtin_amdgcn_s_barrier()
; #define PG8_SCHED __builtin_amdgcn_sched_barrier(0)
; template <class Epi, class Sched, bool ALIGN_EPI = false, bool SP2 = false, bool FP8 = false, bool PEEL = false>
; __device__ __forceinline__ void gemm_phase(PG8_LAS unsigned char* lds, const Gemm g, const Sched& S, const Epi& E, const int wid) {
;     ...
;             const bool last = (t == nt - 2);
;             const char* a1 = cA + (size_t)(t + 1) * kstep;
;             const char* a2 = last ? nA : cA + (size_t)(t + 2) * kstep; const char* b2 = last ? nB : cB + (size_t)(t + 2) * kstep;
;             const char* a3 = a2 + kstep; const char* b3 = b2 + kstep;
;             if (last && has_next) S.a_ready(nxt);
;             PG8_LDB(B0, 0, 0); PG8_LDB(B1, 0, 1); PG8_SCHED; PG8_LDA(At, 0, 0); PG8_STAGE(PG8_SA(1, 1), a1 + hstep, voffA);
;             PG8_WAIT_V(8); PG8_WAIT_L(0); PG8_BAR; PG8_MMA(0, 0, At, B0); PG8_MMA(0, 1, At, B1); PG8_BAR; PG8_SCHED;
.LBB0_1853:
	ds_read_b128 v[0:3], v187
	ds_read_b128 v[4:7], v187 offset:1024
	ds_read_b128 v[16:19], v187 offset:2048
	ds_read_b128 v[20:23], v187 offset:3072
	ds_read_b128 v[24:27], v188
	ds_read_b128 v[28:31], v188 offset:1024
	ds_read_b128 v[176:179], v188 offset:2048
	ds_read_b128 v[180:183], v188 offset:3072
	s_add_u32 s38, s36, 0x200
	s_addc_u32 s39, s37, 0
	s_cmp_eq_u32 s92, 24
	s_cselect_b32 s41, s9, s39
	s_cselect_b32 s40, s8, s38
	s_cselect_b32 s39, s35, s91
	s_cselect_b32 s38, s34, s90
	s_mov_b32 m0, s80
	v_lshl_add_u64 v[216:217], s[36:37], 0, v[170:171]
	ds_read_b128 v[8:11], v186
	ds_read_b128 v[12:15], v186 offset:1024
	ds_read_b128 v[192:195], v186 offset:2048
	ds_read_b128 v[196:199], v186 offset:3072
	ds_read_b128 v[200:203], v186 offset:4096
	ds_read_b128 v[204:207], v186 offset:5120
	ds_read_b128 v[208:211], v186 offset:6144
	ds_read_b128 v[212:215], v186 offset:7168
	global_load_lds_dwordx4 v[216:217], off
	v_lshl_add_u64 v[216:217], s[36:37], 0, v[172:173]
	s_mov_b32 m0, s81
	s_nop 0
	global_load_lds_dwordx4 v[216:217], off
	s_waitcnt vmcnt(8)
	s_waitcnt lgkmcnt(0)
	s_barrier
	s_setprio 1
	s_waitcnt lgkmcnt(0)
	v_mfma_f32_16x16x128_f8f6f4 v[156:159], v[0:7], v[8:15], v[156:159]
	v_mfma_f32_16x16x128_f8f6f4 v[152:155], v[16:23], v[8:15], v[152:155]
	v_mfma_f32_16x16x128_f8f6f4 v[148:151], v[0:7], v[192:199], v[148:151]
	v_mfma_f32_16x16x128_f8f6f4 v[144:147], v[16:23], v[192:199], v[144:147]
	v_mfma_f32_16x16x128_f8f6f4 v[140:143], v[0:7], v[200:207], v[140:143]
	v_mfma_f32_16x16x128_f8f6f4 v[136:139], v[16:23], v[200:207], v[136:139]
	v_mfma_f32_16x16x128_f8f6f4 v[132:135], v[0:7], v[208:215], v[132:135]
	v_mfma_f32_16x16x128_f8f6f4 v[128:131], v[16:23], v[208:215], v[128:131]
	s_setprio 0
	s_setprio 1
	v_mfma_f32_16x16x128_f8f6f4 v[124:127], v[24:31], v[8:15], v[124:127]
	v_mfma_f32_16x16x128_f8f6f4 v[120:123], v[176:183], v[8:15], v[120:123]
	v_mfma_f32_16x16x128_f8f6f4 v[116:119], v[24:31], v[192:199], v[116:119]
	v_mfma_f32_16x16x128_f8f6f4 v[112:115], v[176:183], v[192:199], v[112:115]
	v_mfma_f32_16x16x128_f8f6f4 v[108:111], v[24:31], v[200:207], v[108:111]
	v_mfma_f32_16x16x128_f8f6f4 v[104:107], v[176:183], v[200:207], v[104:107]
	v_mfma_f32_16x16x128_f8f6f4 v[100:103], v[24:31], v[208:215], v[100:103]
	v_mfma_f32_16x16x128_f8f6f4 v[96:99], v[176:183], v[208:215], v[96:99]
	s_setprio 0
	s_barrier
	s_mov_b32 m0, s82
	v_lshl_add_u64 v[8:9], s[38:39], 0, v[162:163]
	s_add_u32 s94, s38, 0x70000
	ds_read_b128 v[192:195], v186 offset:16384
	ds_read_b128 v[196:199], v186 offset:17408
	ds_read_b128 v[200:203], v186 offset:18432
	ds_read_b128 v[204:207], v186 offset:19456
	ds_read_b128 v[208:211], v186 offset:20480
	ds_read_b128 v[212:215], v186 offset:21504
	ds_read_b128 v[216:219], v186 offset:22528
	ds_read_b128 v[220:223], v186 offset:23552
	global_load_lds_dwordx4 v[8:9], off
	v_lshl_add_u64 v[10:11], s[38:39], 0, v[166:167]
	s_mov_b32 m0, s83
	s_addc_u32 s95, s39, 0
	global_load_lds_dwordx4 v[10:11], off
	v_lshl_add_u64 v[12:13], s[94:95], 0, v[162:163]
	s_mov_b32 m0, s84
	v_lshl_add_u64 v[14:15], s[40:41], 0, v[164:165]
	global_load_lds_dwordx4 v[12:13], off
	v_lshl_add_u64 v[12:13], s[94:95], 0, v[166:167]
	s_mov_b32 m0, s85
	s_nop 0
	global_load_lds_dwordx4 v[12:13], off
	v_lshl_add_u64 v[12:13], s[40:41], 0, v[160:161]
	s_mov_b32 m0, s59
	s_nop 0
	global_load_lds_dwordx4 v[12:13], off
	s_mov_b32 m0, s60
	s_nop 0
	global_load_lds_dwordx4 v[14:15], off
	s_waitcnt vmcnt(8)
	s_waitcnt lgkmcnt(0)
	s_barrier
	s_setprio 1
	s_waitcnt lgkmcnt(0)
	v_mfma_f32_16x16x128_f8f6f4 v[92:95], v[0:7], v[192:199], v[92:95]
	v_mfma_f32_16x16x128_f8f6f4 v[88:91], v[16:23], v[192:199], v[88:91]
	v_mfma_f32_16x16x128_f8f6f4 v[84:87], v[0:7], v[200:207], v[84:87]
	v_mfma_f32_16x16x128_f8f6f4 v[80:83], v[16:23], v[200:207], v[80:83]
	v_mfma_f32_16x16x128_f8f6f4 v[76:79], v[0:7], v[208:215], v[76:79]
	v_mfma_f32_16x16x128_f8f6f4 v[72:75], v[16:23], v[208:215], v[72:75]
	v_mfma_f32_16x16x128_f8f6f4 v[68:71], v[0:7], v[216:223], v[68:71]
	v_mfma_f32_16x16x128_f8f6f4 v[64:67], v[16:23], v[216:223], v[64:67]
	s_setprio 0
	s_setprio 1
	v_mfma_f32_16x16x128_f8f6f4 v[60:63], v[24:31], v[192:199], v[60:63]
	v_mfma_f32_16x16x128_f8f6f4 v[56:59], v[176:183], v[192:199], v[56:59]
	v_mfma_f32_16x16x128_f8f6f4 v[52:55], v[24:31], v[200:207], v[52:55]
	v_mfma_f32_16x16x128_f8f6f4 v[48:51], v[176:183], v[200:207], v[48:51]
	v_mfma_f32_16x16x128_f8f6f4 v[44:47], v[24:31], v[208:215], v[44:47]
	v_mfma_f32_16x16x128_f8f6f4 v[40:43], v[176:183], v[208:215], v[40:43]
	v_mfma_f32_16x16x128_f8f6f4 v[36:39], v[24:31], v[216:223], v[36:39]
	v_mfma_f32_16x16x128_f8f6f4 v[32:35], v[176:183], v[216:223], v[32:35]
	s_setprio 0
	s_barrier
; #define PG8_STAGE(bufoff, gbase, voff) do { _Pragma("unroll") for (int _i = 0; _i < 2; ++_i) \
;         __builtin_amdgcn_global_load_lds((const unsigned*)((const char*)(gbase) + (voff)[_i]), (PG8_LAS unsigned*)(lds + (bufoff) + ldsw + _i * 8192), 16, 0, 0); } while (0)
; #define PG8_WAIT_V(n) asm volatile("s_waitcnt vmcnt(" #n ")" ::: "memory")
; #define PG8_WAIT_L(n) asm volatile("s_waitcnt lgkmcnt(" #n ")" ::: "memory")
; #define PG8_BAR __builtin_amdgcn_s_barrier()
; #define PG8_SCHED __builtin_amdgcn_sched_barrier(0)
; template <class Epi, class Sched, bool ALIGN_EPI = false, bool SP2 = false, bool FP8 = false, bool PEEL = false>
; __device__ __forceinline__ void gemm_phase(PG8_LAS unsigned char* lds, const Gemm g, const Sched& S, const Epi& E, const int wid) {
;     ...
;         for (int t = 2; t < nt; t += 2) {
;     ...
;             PG8_LDA(At, 0, 1); PG8_STAGE(PG8_SB(0, 0), b2, voffB); PG8_STAGE(PG8_SB(0, 1), b2 + hstep, voffB); PG8_STAGE(PG8_SA(0, 0), a2, voffA);
;             PG8_WAIT_V(8); PG8_WAIT_L(0); PG8_BAR; PG8_MMA(1, 0, At, B0); PG8_MMA(1, 1, At, B1); PG8_BAR; PG8_SCHED;
;             PG8_LDB(B0, 1, 0); PG8_LDB(B1, 1, 1); PG8_SCHED; PG8_LDA(At, 1, 0); PG8_STAGE(PG8_SA(0, 1), a2 + hstep, voffA);
;             PG8_WAIT_V(8); PG8_WAIT_L(0); PG8_BAR; PG8_MMA(0, 0, At, B0); PG8_MMA(0, 1, At, B1); PG8_BAR; PG8_SCHED;
;             PG8_LDA(At, 1, 1); PG8_STAGE(PG8_SB(1, 0), b3, voffB); PG8_STAGE(PG8_SB(1, 1), b3 + hstep, voffB); PG8_STAGE(PG8_SA(1, 0), a3, voffA);
;             PG8_WAIT_V(8); PG8_WAIT_L(0); PG8_BAR; PG8_MMA(1, 0, At, B0); PG8_MMA(1, 1, At, B1); PG8_BAR; PG8_SCHED;
	ds_read_b128 v[16:19], v189
	ds_read_b128 v[20:23], v189 offset:1024
	ds_read_b128 v[24:27], v189 offset:2048
	ds_read_b128 v[28:31], v189 offset:3072
	ds_read_b128 v[0:3], v190
	ds_read_b128 v[4:7], v190 offset:1024
	ds_read_b128 v[176:179], v190 offset:2048
	ds_read_b128 v[180:183], v190 offset:3072
	s_add_u32 s40, s40, 0x70000
	s_addc_u32 s41, s41, 0
	s_mov_b32 m0, s61
	v_lshl_add_u64 v[224:225], s[40:41], 0, v[160:161]
	ds_read_b128 v[192:195], v186 offset:32768
	ds_read_b128 v[196:199], v186 offset:33792
	ds_read_b128 v[200:203], v186 offset:34816
	ds_read_b128 v[204:207], v186 offset:35840
	ds_read_b128 v[208:211], v186 offset:36864
	ds_read_b128 v[212:215], v186 offset:37888
	ds_read_b128 v[216:219], v186 offset:38912
	ds_read_b128 v[220:223], v186 offset:39936
	global_load_lds_dwordx4 v[224:225], off
	v_lshl_add_u64 v[224:225], s[40:41], 0, v[164:165]
	s_mov_b32 m0, s62
	s_nop 0
	global_load_lds_dwordx4 v[224:225], off
	s_waitcnt vmcnt(8)
	s_waitcnt lgkmcnt(0)
	s_barrier
	s_setprio 1
	s_waitcnt lgkmcnt(0)
	v_mfma_f32_16x16x128_f8f6f4 v[156:159], v[16:23], v[192:199], v[156:159]
	v_mfma_f32_16x16x128_f8f6f4 v[152:155], v[24:31], v[192:199], v[152:155]
	v_mfma_f32_16x16x128_f8f6f4 v[148:151], v[16:23], v[200:207], v[148:151]
	v_mfma_f32_16x16x128_f8f6f4 v[144:147], v[24:31], v[200:207], v[144:147]
	v_mfma_f32_16x16x128_f8f6f4 v[140:143], v[16:23], v[208:215], v[140:143]
	v_mfma_f32_16x16x128_f8f6f4 v[136:139], v[24:31], v[208:215], v[136:139]
	v_mfma_f32_16x16x128_f8f6f4 v[132:135], v[16:23], v[216:223], v[132:135]
	v_mfma_f32_16x16x128_f8f6f4 v[128:131], v[24:31], v[216:223], v[128:131]
	s_setprio 0
	s_setprio 1
	v_mfma_f32_16x16x128_f8f6f4 v[124:127], v[0:7], v[192:199], v[124:127]
	v_mfma_f32_16x16x128_f8f6f4 v[120:123], v[176:183], v[192:199], v[120:123]
	v_mfma_f32_16x16x128_f8f6f4 v[116:119], v[0:7], v[200:207], v[116:119]
	v_mfma_f32_16x16x128_f8f6f4 v[112:115], v[176:183], v[200:207], v[112:115]
	v_mfma_f32_16x16x128_f8f6f4 v[108:111], v[0:7], v[208:215], v[108:111]
	v_mfma_f32_16x16x128_f8f6f4 v[104:107], v[176:183], v[208:215], v[104:107]
	v_mfma_f32_16x16x128_f8f6f4 v[100:103], v[0:7], v[216:223], v[100:103]
	v_mfma_f32_16x16x128_f8f6f4 v[96:99], v[176:183], v[216:223], v[96:99]
	s_setprio 0
	s_barrier
	s_mov_b32 m0, s86
	v_lshl_add_u64 v[8:9], v[8:9], 0, s[22:23]
	s_add_u32 s38, s38, 0x70080
	ds_read_b128 v[192:195], v186 offset:49152
	ds_read_b128 v[196:199], v186 offset:50176
	ds_read_b128 v[200:203], v186 offset:51200
	ds_read_b128 v[204:207], v186 offset:52224
	ds_read_b128 v[208:211], v186 offset:53248
	ds_read_b128 v[212:215], v186 offset:54272
	ds_read_b128 v[216:219], v186 offset:55296
	ds_read_b128 v[220:223], v186 offset:56320
	global_load_lds_dwordx4 v[8:9], off
	v_lshl_add_u64 v[8:9], v[10:11], 0, s[22:23]
	s_mov_b32 m0, s87
	s_addc_u32 s39, s39, 0
	global_load_lds_dwordx4 v[8:9], off
	v_lshl_add_u64 v[8:9], s[38:39], 0, v[162:163]
	s_mov_b32 m0, s88
	s_nop 0
	global_load_lds_dwordx4 v[8:9], off
	v_lshl_add_u64 v[8:9], s[38:39], 0, v[166:167]
	s_mov_b32 m0, s89
	s_nop 0
	global_load_lds_dwordx4 v[8:9], off
	v_lshl_add_u64 v[8:9], v[12:13], 0, s[22:23]
	s_mov_b32 m0, s63
	s_nop 0
	global_load_lds_dwordx4 v[8:9], off
	v_lshl_add_u64 v[8:9], v[14:15], 0, s[22:23]
	s_mov_b32 m0, s64
	s_nop 0
	global_load_lds_dwordx4 v[8:9], off
	s_waitcnt vmcnt(8)
	s_waitcnt lgkmcnt(0)
	s_barrier
	s_setprio 1
	s_waitcnt lgkmcnt(0)
	v_mfma_f32_16x16x128_f8f6f4 v[92:95], v[16:23], v[192:199], v[92:95]
	v_mfma_f32_16x16x128_f8f6f4 v[88:91], v[24:31], v[192:199], v[88:91]
	v_mfma_f32_16x16x128_f8f6f4 v[84:87], v[16:23], v[200:207], v[84:87]
	v_mfma_f32_16x16x128_f8f6f4 v[80:83], v[24:31], v[200:207], v[80:83]
	v_mfma_f32_16x16x128_f8f6f4 v[76:79], v[16:23], v[208:215], v[76:79]
	v_mfma_f32_16x16x128_f8f6f4 v[72:75], v[24:31], v[208:215], v[72:75]
	v_mfma_f32_16x16x128_f8f6f4 v[68:71], v[16:23], v[216:223], v[68:71]
	v_mfma_f32_16x16x128_f8f6f4 v[64:67], v[24:31], v[216:223], v[64:67]
	s_setprio 0
	s_setprio 1
	v_mfma_f32_16x16x128_f8f6f4 v[60:63], v[0:7], v[192:199], v[60:63]
	v_mfma_f32_16x16x128_f8f6f4 v[56:59], v[176:183], v[192:199], v[56:59]
	v_mfma_f32_16x16x128_f8f6f4 v[52:55], v[0:7], v[200:207], v[52:55]
	v_mfma_f32_16x16x128_f8f6f4 v[48:51], v[176:183], v[200:207], v[48:51]
	v_mfma_f32_16x16x128_f8f6f4 v[44:47], v[0:7], v[208:215], v[44:47]
	v_mfma_f32_16x16x128_f8f6f4 v[40:43], v[176:183], v[208:215], v[40:43]
	v_mfma_f32_16x16x128_f8f6f4 v[36:39], v[0:7], v[216:223], v[36:39]
	v_mfma_f32_16x16x128_f8f6f4 v[32:35], v[176:183], v[216:223], v[32:35]
	s_add_i32 s92, s92, 2
	s_add_u32 s36, s36, 0x100
	s_addc_u32 s37, s37, 0
	s_add_u32 s90, s90, 0x100
	s_addc_u32 s91, s91, 0
	s_cmp_gt_u32 s92, 25
	s_setprio 0
	s_barrier
	s_cbranch_scc0 .LBB0_1853
	s_and_b64 vcc, exec, s[12:13]
	s_cbranch_vccz .LBB0_1856
	s_barrier
